# waits to first consumer (7.2) at the remaining block-seam pointer reads (both dword loads before one wait) and mLSTM put_next slots written with ds_write_b64 instead of draining generic stores
# baseline (speedup 1.0000x reference)
.Lstg_b8:
	v_mov_b64_e32 v[144:145], s[70:71]
	flat_load_dword v146, v[144:145] sc0 sc1
	v_mov_b64_e32 v[144:145], s[76:77]
	flat_load_dword v144, v[144:145] sc0 sc1
	s_waitcnt vmcnt(0) lgkmcnt(0)
	v_readfirstlane_b32 s6, v146
	v_readfirstlane_b32 s7, v144
	s_nop 1
	s_nop 3
	s_mov_b32 m0, s81
	s_nop 0
	global_load_lds_dwordx4 v162, s[6:7]
	s_nop 3
	s_add_i32 m0, s78, 0xffffff80
	s_nop 0
	global_load_lds_dwordx4 v162, s[6:7] offset:128
	s_add_i32 m0, s69, 0xffffff00
	s_nop 0
	global_load_lds_dwordx4 v162, s[6:7] offset:256
	s_add_i32 m0, s68, 0xfffffe80
	s_nop 0
	global_load_lds_dwordx4 v162, s[6:7] offset:384
	ds_read_b64_tr_b16 v[144:145], v177 offset:0x8000
	ds_read_b64_tr_b16 v[146:147], v177 offset:0x9000
	ds_read_b64_tr_b16 v[148:149], v177 offset:0xa000
	ds_read_b64_tr_b16 v[150:151], v177 offset:0xb000
	ds_read_b64_tr_b16 v[152:153], v177 offset:0xc000
	ds_read_b64_tr_b16 v[154:155], v177 offset:0xd000
	ds_read_b64_tr_b16 v[156:157], v177 offset:0xe000
	ds_read_b64_tr_b16 v[158:159], v177 offset:0xf000
	ds_read_b64_tr_b16 v[166:167], v177 offset:0x8200
	ds_read_b64_tr_b16 v[168:169], v177 offset:0x9200
	ds_read_b64_tr_b16 v[170:171], v177 offset:0xa200
	ds_read_b64_tr_b16 v[172:173], v177 offset:0xb200
	ds_read_b64_tr_b16 v[180:181], v177 offset:0xc200
	ds_read_b64_tr_b16 v[182:183], v177 offset:0xd200
	ds_read_b64_tr_b16 v[184:185], v177 offset:0xe200
	ds_read_b64_tr_b16 v[186:187], v177 offset:0xf200
	s_waitcnt lgkmcnt(8)
	s_nop 1
	v_mfma_f32_32x32x16_bf16 v[112:127], v[144:147], v[128:131], v[112:127]
	v_mfma_f32_32x32x16_bf16 v[112:127], v[148:151], v[132:135], v[112:127]
	v_mfma_f32_32x32x16_bf16 v[112:127], v[152:155], v[136:139], v[112:127]
	v_mfma_f32_32x32x16_bf16 v[112:127], v[156:159], v[140:143], v[112:127]
	ds_read_b64_tr_b16 v[144:145], v177 offset:0x8400
	ds_read_b64_tr_b16 v[146:147], v177 offset:0x9400
	ds_read_b64_tr_b16 v[148:149], v177 offset:0xa400
	ds_read_b64_tr_b16 v[150:151], v177 offset:0xb400
	ds_read_b64_tr_b16 v[152:153], v177 offset:0xc400
	ds_read_b64_tr_b16 v[154:155], v177 offset:0xd400
	ds_read_b64_tr_b16 v[156:157], v177 offset:0xe400
	ds_read_b64_tr_b16 v[158:159], v177 offset:0xf400
	s_waitcnt lgkmcnt(8)
	v_mfma_f32_32x32x16_bf16 v[0:15], v[166:169], v[128:131], v[0:15]
	v_mfma_f32_32x32x16_bf16 v[0:15], v[170:173], v[132:135], v[0:15]
	v_mfma_f32_32x32x16_bf16 v[0:15], v[180:183], v[136:139], v[0:15]
	v_mfma_f32_32x32x16_bf16 v[0:15], v[184:187], v[140:143], v[0:15]
	ds_read_b64_tr_b16 v[166:167], v177 offset:0x8600
	ds_read_b64_tr_b16 v[168:169], v177 offset:0x9600
	ds_read_b64_tr_b16 v[170:171], v177 offset:0xa600
	ds_read_b64_tr_b16 v[172:173], v177 offset:0xb600
	ds_read_b64_tr_b16 v[180:181], v177 offset:0xc600
	ds_read_b64_tr_b16 v[182:183], v177 offset:0xd600
	ds_read_b64_tr_b16 v[184:185], v177 offset:0xe600
	ds_read_b64_tr_b16 v[186:187], v177 offset:0xf600
	s_waitcnt lgkmcnt(8)
	v_mfma_f32_32x32x16_bf16 v[16:31], v[144:147], v[128:131], v[16:31]
	v_mfma_f32_32x32x16_bf16 v[16:31], v[148:151], v[132:135], v[16:31]
	v_mfma_f32_32x32x16_bf16 v[16:31], v[152:155], v[136:139], v[16:31]
	v_mfma_f32_32x32x16_bf16 v[16:31], v[156:159], v[140:143], v[16:31]
	ds_read_b64_tr_b16 v[144:145], v177 offset:0x8800
	ds_read_b64_tr_b16 v[146:147], v177 offset:0x9800
	ds_read_b64_tr_b16 v[148:149], v177 offset:0xa800
	ds_read_b64_tr_b16 v[150:151], v177 offset:0xb800
	ds_read_b64_tr_b16 v[152:153], v177 offset:0xc800
	ds_read_b64_tr_b16 v[154:155], v177 offset:0xd800
	ds_read_b64_tr_b16 v[156:157], v177 offset:0xe800
	ds_read_b64_tr_b16 v[158:159], v177 offset:0xf800
	s_waitcnt lgkmcnt(8)
	v_mfma_f32_32x32x16_bf16 v[32:47], v[166:169], v[128:131], v[32:47]
	v_mfma_f32_32x32x16_bf16 v[32:47], v[170:173], v[132:135], v[32:47]
	v_mfma_f32_32x32x16_bf16 v[32:47], v[180:183], v[136:139], v[32:47]
	v_mfma_f32_32x32x16_bf16 v[32:47], v[184:187], v[140:143], v[32:47]
	ds_read_b64_tr_b16 v[166:167], v177 offset:0x8a00
	ds_read_b64_tr_b16 v[168:169], v177 offset:0x9a00
	ds_read_b64_tr_b16 v[170:171], v177 offset:0xaa00
	ds_read_b64_tr_b16 v[172:173], v177 offset:0xba00
	ds_read_b64_tr_b16 v[180:181], v177 offset:0xca00
	ds_read_b64_tr_b16 v[182:183], v177 offset:0xda00
	ds_read_b64_tr_b16 v[184:185], v177 offset:0xea00
	ds_read_b64_tr_b16 v[186:187], v177 offset:0xfa00
	s_waitcnt lgkmcnt(8)
	v_mfma_f32_32x32x16_bf16 v[48:63], v[144:147], v[128:131], v[48:63]
	v_mfma_f32_32x32x16_bf16 v[48:63], v[148:151], v[132:135], v[48:63]
	v_mfma_f32_32x32x16_bf16 v[48:63], v[152:155], v[136:139], v[48:63]
	v_mfma_f32_32x32x16_bf16 v[48:63], v[156:159], v[140:143], v[48:63]
	ds_read_b64_tr_b16 v[144:145], v177 offset:0x8c00
	ds_read_b64_tr_b16 v[146:147], v177 offset:0x9c00
	ds_read_b64_tr_b16 v[148:149], v177 offset:0xac00
	ds_read_b64_tr_b16 v[150:151], v177 offset:0xbc00
	ds_read_b64_tr_b16 v[152:153], v177 offset:0xcc00
	ds_read_b64_tr_b16 v[154:155], v177 offset:0xdc00
	ds_read_b64_tr_b16 v[156:157], v177 offset:0xec00
	ds_read_b64_tr_b16 v[158:159], v177 offset:0xfc00
	s_waitcnt lgkmcnt(8)
	v_mfma_f32_32x32x16_bf16 v[64:79], v[166:169], v[128:131], v[64:79]
	v_mfma_f32_32x32x16_bf16 v[64:79], v[170:173], v[132:135], v[64:79]
	v_mfma_f32_32x32x16_bf16 v[64:79], v[180:183], v[136:139], v[64:79]
	v_mfma_f32_32x32x16_bf16 v[64:79], v[184:187], v[140:143], v[64:79]
	ds_read_b64_tr_b16 v[166:167], v177 offset:0x8e00
	ds_read_b64_tr_b16 v[168:169], v177 offset:0x9e00
	ds_read_b64_tr_b16 v[170:171], v177 offset:0xae00
	ds_read_b64_tr_b16 v[172:173], v177 offset:0xbe00
	ds_read_b64_tr_b16 v[180:181], v177 offset:0xce00
	ds_read_b64_tr_b16 v[182:183], v177 offset:0xde00
	ds_read_b64_tr_b16 v[184:185], v177 offset:0xee00
	ds_read_b64_tr_b16 v[186:187], v177 offset:0xfe00
	s_waitcnt lgkmcnt(8)
	v_mfma_f32_32x32x16_bf16 v[80:95], v[144:147], v[128:131], v[80:95]
	v_mfma_f32_32x32x16_bf16 v[80:95], v[148:151], v[132:135], v[80:95]
	v_mfma_f32_32x32x16_bf16 v[80:95], v[152:155], v[136:139], v[80:95]
	v_mfma_f32_32x32x16_bf16 v[80:95], v[156:159], v[140:143], v[80:95]
	s_waitcnt lgkmcnt(0)
	v_mfma_f32_32x32x16_bf16 v[96:111], v[166:169], v[128:131], v[96:111]
	v_mfma_f32_32x32x16_bf16 v[96:111], v[170:173], v[132:135], v[96:111]
	v_mfma_f32_32x32x16_bf16 v[96:111], v[180:183], v[136:139], v[96:111]
	v_mfma_f32_32x32x16_bf16 v[96:111], v[184:187], v[140:143], v[96:111]
	v_readlane_b32 s6, v255, 31
	v_readlane_b32 s7, v255, 32
	v_readlane_b32 s12, v255, 49
	v_readlane_b32 s13, v255, 50
	v_mov_b64_e32 v[128:129], s[6:7]
	v_readlane_b32 s6, v255, 35
	v_readlane_b32 s7, v255, 36
	flat_load_dword v130, v[128:129] sc0 sc1
	s_ashr_i32 s13, s12, 31
	v_mov_b64_e32 v[128:129], s[6:7]
	flat_load_dword v131, v[128:129] sc0 sc1
	s_waitcnt vmcnt(0)
	s_lshl_b64 s[6:7], s[12:13], 11
	v_lshl_or_b32 v128, v175, 11, v174
	v_mov_b32_e32 v129, v161
	s_waitcnt lgkmcnt(0)
	s_barrier
	v_add_f32_e32 v158, v179, v204
	s_waitcnt lgkmcnt(0)
	v_readfirstlane_b32 s9, v130
	s_add_u32 s6, s9, s6
	v_readfirstlane_b32 s8, v131
	s_addc_u32 s7, s8, s7
	v_lshl_add_u64 v[156:157], s[6:7], 0, v[128:129]
	flat_load_dwordx4 v[128:131], v[156:157]
	flat_load_dwordx4 v[132:135], v[156:157] offset:32
	flat_load_dwordx4 v[136:139], v[156:157] offset:64
	flat_load_dwordx4 v[140:143], v[156:157] offset:96
	flat_load_dwordx4 v[144:147], v[156:157] offset:128
	flat_load_dwordx4 v[148:151], v[156:157] offset:160
	flat_load_dwordx4 v[152:155], v[156:157] offset:192
	flat_load_dwordx4 v[166:169], v[156:157] offset:224
	v_readlane_b32 s6, v255, 51
	v_readlane_b32 s7, v255, 52
	s_add_u32 s4, s4, s6
	s_addc_u32 s5, s5, s7
	v_lshl_add_u64 v[156:157], s[4:5], 0, v[160:161]
	flat_load_dword v156, v[156:157]
	v_mov_b32_e32 v157, v158
	s_nop 1
	v_permlane32_swap_b32_e32 v158, v157
	v_add_f32_e32 v157, v158, v157
	s_mul_i32 s5, s12, 0x6800
	s_mul_hi_i32 s4, s12, 0x6800
	s_add_u32 s2, s2, s5
	s_addc_u32 s3, s3, s4
	s_add_u32 s4, s2, 0x1000
	s_addc_u32 s5, s3, 0
	v_readlane_b32 s2, v255, 27
	s_waitcnt vmcnt(0) lgkmcnt(0)
	v_max_f32_e32 v156, v156, v156
	v_max_f32_e64 v156, |v157|, v156
	v_rcp_f32_e32 v194, v156
	s_nop 0
	v_mul_f32_e32 v196, v113, v194
	v_mul_f32_e32 v213, v115, v194
	v_mul_f32_e32 v195, v112, v194
	v_mul_f32_e32 v197, v114, v194
	v_mul_f32_e32 v217, v119, v194
	v_mul_f32_e32 v119, v52, v194
	v_mul_f32_e32 v115, v54, v194
	v_mul_f32_e32 v54, v56, v194
	v_mul_f32_e32 v52, v57, v194
	v_mul_f32_e32 v56, v196, v196
	v_mul_f32_e32 v57, v213, v213
	v_mul_f32_e32 v215, v117, v194
	v_fmac_f32_e32 v56, v195, v195
	v_fmac_f32_e32 v57, v197, v197
	v_mul_f32_e32 v214, v116, v194
	v_mul_f32_e32 v216, v118, v194
	v_mul_f32_e32 v114, v50, v194
	v_mul_f32_e32 v50, v58, v194
	v_add_f32_e32 v56, v56, v57
	v_mul_f32_e32 v57, v215, v215
	v_mul_f32_e32 v58, v217, v217
	v_mul_f32_e32 v219, v121, v194
	v_mul_f32_e32 v210, v123, v194
	v_fmac_f32_e32 v57, v214, v214
	v_fmac_f32_e32 v58, v216, v216
	v_mul_f32_e32 v218, v120, v194
	v_mul_f32_e32 v212, v122, v194
	v_mul_f32_e32 v118, v48, v194
	v_mul_f32_e32 v48, v59, v194
	v_add_f32_e32 v57, v57, v58
	v_mul_f32_e32 v58, v219, v219
	v_mul_f32_e32 v59, v210, v210
	v_mul_f32_e32 v221, v125, v194
	v_mul_f32_e32 v211, v127, v194
	v_fmac_f32_e32 v58, v218, v218
	v_fmac_f32_e32 v59, v212, v212
	v_mul_f32_e32 v220, v124, v194
	v_mul_f32_e32 v222, v126, v194
	v_mul_f32_e32 v113, v55, v194
	v_mul_f32_e32 v55, v60, v194
	v_add_f32_e32 v58, v58, v59
	v_mul_f32_e32 v59, v221, v221
	v_mul_f32_e32 v60, v211, v211
	v_fmac_f32_e32 v59, v220, v220
	v_fmac_f32_e32 v60, v222, v222
	v_add_f32_e32 v59, v59, v60
	v_mul_f32_e32 v206, v1, v194
	v_mul_f32_e32 v202, v3, v194
	v_add_f32_e32 v56, v56, v57
	v_add_f32_e32 v57, v58, v59
	v_mul_f32_e32 v208, v0, v194
	v_mul_f32_e32 v204, v2, v194
	v_add_f32_e32 v56, v56, v57
	v_mul_f32_e32 v57, v206, v206
	v_mul_f32_e32 v58, v202, v202
	v_mul_f32_e32 v207, v5, v194
	v_mul_f32_e32 v203, v7, v194
	v_fmac_f32_e32 v57, v208, v208
	v_fmac_f32_e32 v58, v204, v204
	v_mul_f32_e32 v209, v4, v194
	v_mul_f32_e32 v205, v6, v194
	v_add_f32_e32 v57, v57, v58
	v_mul_f32_e32 v58, v207, v207
	v_mul_f32_e32 v59, v203, v203
	v_mul_f32_e32 v198, v9, v194
	v_mul_f32_e32 v190, v11, v194
	v_fmac_f32_e32 v58, v209, v209
	v_fmac_f32_e32 v59, v205, v205
	v_mul_f32_e32 v200, v8, v194
	v_mul_f32_e32 v192, v10, v194
	v_add_f32_e32 v58, v58, v59
	v_mul_f32_e32 v59, v198, v198
	v_mul_f32_e32 v60, v190, v190
	v_mul_f32_e32 v199, v13, v194
	v_mul_f32_e32 v191, v15, v194
	v_fmac_f32_e32 v59, v200, v200
	v_fmac_f32_e32 v60, v192, v192
	v_mul_f32_e32 v201, v12, v194
	v_mul_f32_e32 v193, v14, v194
	v_mul_f32_e32 v117, v53, v194
	v_mul_f32_e32 v53, v61, v194
	v_add_f32_e32 v59, v59, v60
	v_mul_f32_e32 v60, v199, v199
	v_mul_f32_e32 v61, v191, v191
	v_fmac_f32_e32 v60, v201, v201
	v_fmac_f32_e32 v61, v193, v193
	v_add_f32_e32 v60, v60, v61
	v_add_f32_e32 v57, v57, v58
	v_add_f32_e32 v58, v59, v60
	v_mul_f32_e32 v186, v17, v194
	v_mul_f32_e32 v182, v19, v194
	v_add_f32_e32 v57, v57, v58
	v_mul_f32_e32 v188, v16, v194
	v_mul_f32_e32 v184, v18, v194
	v_add_f32_e32 v56, v56, v57
	v_mul_f32_e32 v57, v186, v186
	v_mul_f32_e32 v58, v182, v182
	v_mul_f32_e32 v187, v21, v194
	v_mul_f32_e32 v183, v23, v194
	v_fmac_f32_e32 v57, v188, v188
	v_fmac_f32_e32 v58, v184, v184
	v_mul_f32_e32 v189, v20, v194
	v_mul_f32_e32 v185, v22, v194
	v_add_f32_e32 v57, v57, v58
	v_mul_f32_e32 v58, v187, v187
	v_mul_f32_e32 v59, v183, v183
	v_mul_f32_e32 v178, v25, v194
	v_mul_f32_e32 v171, v27, v194
	v_fmac_f32_e32 v58, v189, v189
	v_fmac_f32_e32 v59, v185, v185
	v_mul_f32_e32 v180, v24, v194
	v_mul_f32_e32 v173, v26, v194
	v_add_f32_e32 v58, v58, v59
	v_mul_f32_e32 v59, v178, v178
	v_mul_f32_e32 v60, v171, v171
	v_mul_f32_e32 v179, v29, v194
	v_mul_f32_e32 v172, v31, v194
	v_fmac_f32_e32 v59, v180, v180
	v_fmac_f32_e32 v60, v173, v173
	v_mul_f32_e32 v181, v28, v194
	v_mul_f32_e32 v177, v30, v194
	v_add_f32_e32 v59, v59, v60
	v_mul_f32_e32 v60, v179, v179
	v_mul_f32_e32 v61, v172, v172
	v_fmac_f32_e32 v60, v181, v181
	v_fmac_f32_e32 v61, v177, v177
	v_add_f32_e32 v60, v60, v61
	v_add_f32_e32 v57, v57, v58
	v_add_f32_e32 v58, v59, v60
	v_mul_f32_e32 v160, v33, v194
	v_mul_f32_e32 v156, v35, v194
	v_add_f32_e32 v57, v57, v58
	v_mul_f32_e32 v163, v32, v194
	v_mul_f32_e32 v158, v34, v194
	v_add_f32_e32 v56, v57, v56
	v_mul_f32_e32 v57, v160, v160
	v_mul_f32_e32 v58, v156, v156
	v_mul_f32_e32 v162, v37, v194
	v_mul_f32_e32 v157, v39, v194
	v_fmac_f32_e32 v57, v163, v163
	v_fmac_f32_e32 v58, v158, v158
	v_mul_f32_e32 v170, v36, v194
	v_mul_f32_e32 v159, v38, v194
	v_add_f32_e32 v57, v57, v58
	v_mul_f32_e32 v58, v162, v162
	v_mul_f32_e32 v59, v157, v157
	v_mul_f32_e32 v124, v41, v194
	v_mul_f32_e32 v120, v43, v194
	v_fmac_f32_e32 v58, v170, v170
	v_fmac_f32_e32 v59, v159, v159
	v_mul_f32_e32 v126, v40, v194
	v_mul_f32_e32 v122, v42, v194
	v_add_f32_e32 v58, v58, v59
	v_mul_f32_e32 v59, v124, v124
	v_mul_f32_e32 v60, v120, v120
	v_mul_f32_e32 v125, v45, v194
	v_mul_f32_e32 v121, v47, v194
	v_fmac_f32_e32 v59, v126, v126
	v_fmac_f32_e32 v60, v122, v122
	v_mul_f32_e32 v127, v44, v194
	v_mul_f32_e32 v123, v46, v194
	v_add_f32_e32 v59, v59, v60
	v_mul_f32_e32 v60, v125, v125
	v_mul_f32_e32 v61, v121, v121
	v_fmac_f32_e32 v60, v127, v127
	v_fmac_f32_e32 v61, v123, v123
	v_add_f32_e32 v60, v60, v61
	v_add_f32_e32 v57, v57, v58
	v_add_f32_e32 v58, v59, v60
	v_mul_f32_e32 v116, v49, v194
	v_mul_f32_e32 v112, v51, v194
	v_add_f32_e32 v57, v57, v58
	v_add_f32_e32 v56, v57, v56
	v_mul_f32_e32 v57, v116, v116
	v_mul_f32_e32 v58, v112, v112
	v_fmac_f32_e32 v57, v118, v118
	v_fmac_f32_e32 v58, v114, v114
	v_add_f32_e32 v57, v57, v58
	v_mul_f32_e32 v58, v117, v117
	v_mul_f32_e32 v59, v113, v113
	v_fmac_f32_e32 v58, v119, v119
	v_fmac_f32_e32 v59, v115, v115
	v_add_f32_e32 v58, v58, v59
	v_mul_f32_e32 v59, v52, v52
	v_mul_f32_e32 v60, v48, v48
	v_mul_f32_e32 v49, v63, v194
	v_fmac_f32_e32 v59, v54, v54
	v_fmac_f32_e32 v60, v50, v50
	v_mul_f32_e32 v51, v62, v194
	v_add_f32_e32 v59, v59, v60
	v_mul_f32_e32 v60, v53, v53
	v_mul_f32_e32 v61, v49, v49
	v_fmac_f32_e32 v60, v55, v55
	v_fmac_f32_e32 v61, v51, v51
	v_add_f32_e32 v60, v60, v61
	v_add_f32_e32 v57, v57, v58
	v_add_f32_e32 v58, v59, v60
	v_mul_f32_e32 v44, v65, v194
	v_mul_f32_e32 v40, v67, v194
	v_add_f32_e32 v57, v57, v58
	v_mul_f32_e32 v46, v64, v194
	v_mul_f32_e32 v42, v66, v194
	v_add_f32_e32 v56, v57, v56
	v_mul_f32_e32 v57, v44, v44
	v_mul_f32_e32 v58, v40, v40
	v_mul_f32_e32 v45, v69, v194
	v_mul_f32_e32 v41, v71, v194
	v_fmac_f32_e32 v57, v46, v46
	v_fmac_f32_e32 v58, v42, v42
	v_mul_f32_e32 v47, v68, v194
	v_mul_f32_e32 v43, v70, v194
	v_add_f32_e32 v57, v57, v58
	v_mul_f32_e32 v58, v45, v45
	v_mul_f32_e32 v59, v41, v41
	v_mul_f32_e32 v36, v73, v194
	v_mul_f32_e32 v32, v75, v194
	v_fmac_f32_e32 v58, v47, v47
	v_fmac_f32_e32 v59, v43, v43
	v_mul_f32_e32 v38, v72, v194
	v_mul_f32_e32 v34, v74, v194
	v_add_f32_e32 v58, v58, v59
	v_mul_f32_e32 v59, v36, v36
	v_mul_f32_e32 v60, v32, v32
	v_mul_f32_e32 v37, v77, v194
	v_mul_f32_e32 v33, v79, v194
	v_fmac_f32_e32 v59, v38, v38
	v_fmac_f32_e32 v60, v34, v34
	v_mul_f32_e32 v39, v76, v194
	v_mul_f32_e32 v35, v78, v194
	v_add_f32_e32 v59, v59, v60
	v_mul_f32_e32 v60, v37, v37
	v_mul_f32_e32 v61, v33, v33
	v_fmac_f32_e32 v60, v39, v39
	v_fmac_f32_e32 v61, v35, v35
	v_mul_f32_e32 v31, v84, v194
	v_add_f32_e32 v60, v60, v61
	v_mul_u32_u24_e32 v84, 0x6800, v175
	v_add_f32_e32 v57, v57, v58
	v_add_f32_e32 v58, v59, v60
	v_lshl_or_b32 v59, v176, 3, v84
	global_load_dwordx2 v[68:69], v59, s[4:5]
	global_load_dwordx2 v[70:71], v59, s[4:5] offset:16
	global_load_dwordx2 v[72:73], v59, s[4:5] offset:32
	global_load_dwordx2 v[74:75], v59, s[4:5] offset:48
	v_mul_f32_e32 v30, v80, v194
	v_mul_f32_e32 v28, v81, v194
	v_mul_f32_e32 v26, v82, v194
	v_mul_f32_e32 v24, v83, v194
	v_add_f32_e32 v57, v57, v58
	global_load_dwordx2 v[76:77], v59, s[4:5] offset:64
	global_load_dwordx2 v[78:79], v59, s[4:5] offset:80
	global_load_dwordx2 v[80:81], v59, s[4:5] offset:96
	global_load_dwordx2 v[82:83], v59, s[4:5] offset:112
	v_add_f32_e32 v56, v57, v56
	v_mul_f32_e32 v57, v28, v28
	v_mul_f32_e32 v58, v24, v24
	v_mul_f32_e32 v29, v85, v194
	v_mul_f32_e32 v25, v87, v194
	v_fmac_f32_e32 v57, v30, v30
	v_fmac_f32_e32 v58, v26, v26
	v_mul_f32_e32 v27, v86, v194
	v_add_f32_e32 v57, v57, v58
	v_mul_f32_e32 v58, v29, v29
	v_mul_f32_e32 v60, v25, v25
	v_mul_f32_e32 v20, v89, v194
	v_mul_f32_e32 v16, v91, v194
	v_fmac_f32_e32 v58, v31, v31
	v_fmac_f32_e32 v60, v27, v27
	v_mul_f32_e32 v22, v88, v194
	v_mul_f32_e32 v18, v90, v194
	v_add_f32_e32 v58, v58, v60
	v_mul_f32_e32 v60, v20, v20
	v_mul_f32_e32 v61, v16, v16
	v_mul_f32_e32 v21, v93, v194
	v_mul_f32_e32 v17, v95, v194
	v_fmac_f32_e32 v60, v22, v22
	v_fmac_f32_e32 v61, v18, v18
	v_mul_f32_e32 v23, v92, v194
	v_mul_f32_e32 v19, v94, v194
	v_add_f32_e32 v60, v60, v61
	v_mul_f32_e32 v61, v21, v21
	v_mul_f32_e32 v62, v17, v17
	v_fmac_f32_e32 v61, v23, v23
	v_fmac_f32_e32 v62, v19, v19
	v_add_f32_e32 v61, v61, v62
	v_add_f32_e32 v57, v57, v58
	v_add_f32_e32 v58, v60, v61
	v_mul_f32_e32 v12, v97, v194
	v_mul_f32_e32 v8, v99, v194
	v_add_f32_e32 v57, v57, v58
	v_mul_f32_e32 v14, v96, v194
	v_mul_f32_e32 v10, v98, v194
	v_add_f32_e32 v56, v57, v56
	v_mul_f32_e32 v57, v12, v12
	v_mul_f32_e32 v58, v8, v8
	v_mul_f32_e32 v13, v101, v194
	v_mul_f32_e32 v9, v103, v194
	v_fmac_f32_e32 v57, v14, v14
	v_fmac_f32_e32 v58, v10, v10
	v_mul_f32_e32 v15, v100, v194
	v_mul_f32_e32 v11, v102, v194
	v_add_f32_e32 v57, v57, v58
	v_mul_f32_e32 v58, v13, v13
	v_mul_f32_e32 v60, v9, v9
	v_mul_f32_e32 v4, v105, v194
	v_mul_f32_e32 v0, v107, v194
	v_fmac_f32_e32 v58, v15, v15
	v_fmac_f32_e32 v60, v11, v11
	v_mul_f32_e32 v6, v104, v194
	v_mul_f32_e32 v2, v106, v194
	v_add_f32_e32 v58, v58, v60
	v_mul_f32_e32 v60, v4, v4
	v_mul_f32_e32 v61, v0, v0
	v_mul_f32_e32 v5, v109, v194
	v_mul_f32_e32 v1, v111, v194
	v_fmac_f32_e32 v60, v6, v6
	v_fmac_f32_e32 v61, v2, v2
	v_mul_f32_e32 v7, v108, v194
	v_mul_f32_e32 v3, v110, v194
	v_add_f32_e32 v60, v60, v61
	v_mul_f32_e32 v61, v5, v5
	v_mul_f32_e32 v62, v1, v1
	v_fmac_f32_e32 v61, v7, v7
	v_fmac_f32_e32 v62, v3, v3
	v_add_f32_e32 v61, v61, v62
	v_add_f32_e32 v57, v57, v58
	v_add_f32_e32 v58, v60, v61
	v_add_f32_e32 v57, v57, v58
	v_add_f32_e32 v56, v57, v56
	v_mov_b32_e32 v57, v56
	s_nop 1
	v_permlane32_swap_b32_e32 v56, v57
	v_add_f32_e32 v56, v56, v57
	v_fmamk_f32 v56, v56, 0x3b800000, v254
	v_rsq_f32_e32 v56, v56
	v_add_u32_e32 v57, s2, v174
	ds_read_b128 v[60:63], v57
	ds_read_b128 v[64:67], v57 offset:32
	v_mul_f32_e32 v58, v195, v56
	v_mul_f32_e32 v54, v54, v56
	v_mul_f32_e32 v52, v52, v56
	s_waitcnt lgkmcnt(1)
	v_mul_f32_e32 v58, v58, v60
	v_mul_f32_e32 v60, v214, v56
	s_waitcnt lgkmcnt(0)
	v_mul_f32_e32 v60, v60, v64
	v_mul_f32_e32 v64, v196, v56
	v_mul_f32_e32 v61, v64, v61
	v_mul_f32_e32 v64, v215, v56
	v_mul_f32_e32 v64, v64, v65
	v_mul_f32_e32 v65, v197, v56
	v_mul_f32_e32 v62, v65, v62
	v_mul_f32_e32 v65, v216, v56
	v_mul_f32_e32 v65, v65, v66
	v_mul_f32_e32 v66, v213, v56
	v_mul_f32_e32 v63, v66, v63
	v_mul_f32_e32 v66, v217, v56
	v_mul_f32_e32 v66, v66, v67
	s_waitcnt vmcnt(7)
	v_lshlrev_b32_e32 v67, 16, v68
	v_mul_f32_e32 v58, v58, v67
	v_and_b32_e32 v67, 0xffff0000, v68
	v_mul_f32_e32 v61, v61, v67
	v_lshlrev_b32_e32 v67, 16, v69
	v_mul_f32_e32 v62, v62, v67
	v_and_b32_e32 v67, 0xffff0000, v69
	v_mul_f32_e32 v63, v63, v67
	s_waitcnt vmcnt(6)
	v_lshlrev_b32_e32 v67, 16, v70
	v_mul_f32_e32 v67, v60, v67
	v_and_b32_e32 v60, 0xffff0000, v70
	v_mul_f32_e32 v64, v64, v60
	v_lshlrev_b32_e32 v60, 16, v71
	v_mul_f32_e32 v65, v65, v60
	v_and_b32_e32 v60, 0xffff0000, v71
	v_mul_f32_e32 v66, v66, v60
	v_cvt_pk_bf16_f32 v60, v58, v61
	v_cvt_pk_bf16_f32 v61, v62, v63
	v_cvt_pk_bf16_f32 v62, v67, v64
	v_cvt_pk_bf16_f32 v63, v65, v66
	ds_read_b128 v[64:67], v57 offset:64
	ds_read_b128 v[68:71], v57 offset:96
	v_permlane32_swap_b32_e32 v60, v62
	v_permlane32_swap_b32_e32 v61, v63
	v_or_b32_e32 v58, v174, v84
	global_store_dwordx4 v58, v[60:63], s[4:5]
	v_mul_f32_e32 v50, v50, v56
	v_mul_f32_e32 v48, v48, v56
	v_mul_f32_e32 v60, v218, v56
	v_mul_f32_e32 v61, v220, v56
	s_waitcnt lgkmcnt(1)
	v_mul_f32_e32 v60, v60, v64
	s_waitcnt lgkmcnt(0)
	v_mul_f32_e32 v61, v61, v68
	v_mul_f32_e32 v62, v219, v56
	s_waitcnt vmcnt(6)
	v_lshlrev_b32_e32 v68, 16, v72
	v_mul_f32_e32 v62, v62, v65
	v_mul_f32_e32 v64, v212, v56
	v_mul_f32_e32 v60, v60, v68
	v_and_b32_e32 v68, 0xffff0000, v72
	v_mul_f32_e32 v64, v64, v66
	v_mul_f32_e32 v66, v210, v56
	v_mul_f32_e32 v62, v62, v68
	v_lshlrev_b32_e32 v68, 16, v73
	v_mul_f32_e32 v66, v66, v67
	v_mul_f32_e32 v64, v64, v68
	v_and_b32_e32 v68, 0xffff0000, v73
	v_mul_f32_e32 v63, v221, v56
	v_mul_f32_e32 v66, v66, v68
	s_waitcnt vmcnt(5)
	v_lshlrev_b32_e32 v68, 16, v74
	v_mul_f32_e32 v63, v63, v69
	v_mul_f32_e32 v65, v222, v56
	v_mul_f32_e32 v68, v61, v68
	v_and_b32_e32 v61, 0xffff0000, v74
	v_mul_f32_e32 v65, v65, v70
	v_mul_f32_e32 v67, v211, v56
	v_mul_f32_e32 v63, v63, v61
	v_lshlrev_b32_e32 v61, 16, v75
	v_mul_f32_e32 v67, v67, v71
	v_mul_f32_e32 v65, v65, v61
	v_and_b32_e32 v61, 0xffff0000, v75
	v_mul_f32_e32 v67, v67, v61
	v_cvt_pk_bf16_f32 v60, v60, v62
	v_cvt_pk_bf16_f32 v61, v64, v66
	v_cvt_pk_bf16_f32 v62, v68, v63
	v_cvt_pk_bf16_f32 v63, v65, v67
	v_mul_f32_e32 v68, v208, v56
	v_permlane32_swap_b32_e32 v60, v62
	v_permlane32_swap_b32_e32 v61, v63
	global_store_dwordx4 v58, v[60:63], s[4:5] offset:32
	global_load_dwordx2 v[72:73], v59, s[4:5] offset:128
	global_load_dwordx2 v[74:75], v59, s[4:5] offset:144
	global_load_dwordx2 v[84:85], v59, s[4:5] offset:160
	global_load_dwordx2 v[86:87], v59, s[4:5] offset:176
	ds_read_b128 v[60:63], v57 offset:128
	ds_read_b128 v[64:67], v57 offset:160
	v_mul_f32_e32 v55, v55, v56
	v_mul_f32_e32 v53, v53, v56
	v_mul_f32_e32 v51, v51, v56
	s_waitcnt lgkmcnt(1)
	v_mul_f32_e32 v60, v68, v60
	v_mul_f32_e32 v68, v209, v56
	s_waitcnt lgkmcnt(0)
	v_mul_f32_e32 v64, v68, v64
	v_mul_f32_e32 v68, v206, v56
	v_mul_f32_e32 v61, v68, v61
	v_mul_f32_e32 v68, v207, v56
	v_mul_f32_e32 v65, v68, v65
	v_mul_f32_e32 v68, v204, v56
	v_mul_f32_e32 v62, v68, v62
	v_mul_f32_e32 v68, v205, v56
	v_mul_f32_e32 v66, v68, v66
	v_mul_f32_e32 v68, v202, v56
	v_mul_f32_e32 v63, v68, v63
	v_mul_f32_e32 v68, v203, v56
	v_mul_f32_e32 v67, v68, v67
	s_waitcnt vmcnt(9)
	v_lshlrev_b32_e32 v68, 16, v76
	v_mul_f32_e32 v60, v60, v68
	v_and_b32_e32 v68, 0xffff0000, v76
	v_mul_f32_e32 v61, v61, v68
	v_lshlrev_b32_e32 v68, 16, v77
	v_mul_f32_e32 v62, v62, v68
	v_and_b32_e32 v68, 0xffff0000, v77
	v_mul_f32_e32 v63, v63, v68
	s_waitcnt vmcnt(8)
	v_lshlrev_b32_e32 v68, 16, v78
	v_mul_f32_e32 v64, v64, v68
	v_and_b32_e32 v68, 0xffff0000, v78
	v_mul_f32_e32 v65, v65, v68
	v_lshlrev_b32_e32 v68, 16, v79
	v_mul_f32_e32 v66, v66, v68
	v_and_b32_e32 v68, 0xffff0000, v79
	v_mul_f32_e32 v67, v67, v68
	v_cvt_pk_bf16_f32 v60, v60, v61
	v_cvt_pk_bf16_f32 v61, v62, v63
	v_cvt_pk_bf16_f32 v62, v64, v65
	v_cvt_pk_bf16_f32 v63, v66, v67
	ds_read_b128 v[64:67], v57 offset:192
	ds_read_b128 v[68:71], v57 offset:224
	v_permlane32_swap_b32_e32 v60, v62
	v_permlane32_swap_b32_e32 v61, v63
	global_store_dwordx4 v58, v[60:63], s[4:5] offset:64
	v_mul_f32_e32 v49, v49, v56
	v_mul_f32_e32 v46, v46, v56
	v_mul_f32_e32 v60, v200, v56
	v_mul_f32_e32 v61, v201, v56
	s_waitcnt lgkmcnt(1)
	v_mul_f32_e32 v60, v60, v64
	s_waitcnt lgkmcnt(0)
	v_mul_f32_e32 v61, v61, v68
	v_mul_f32_e32 v62, v198, v56
	s_waitcnt vmcnt(8)
	v_lshlrev_b32_e32 v68, 16, v80
	v_mul_f32_e32 v62, v62, v65
	v_mul_f32_e32 v64, v192, v56
	v_mul_f32_e32 v60, v60, v68
	v_and_b32_e32 v68, 0xffff0000, v80
	v_mul_f32_e32 v64, v64, v66
	v_mul_f32_e32 v66, v190, v56
	v_mul_f32_e32 v62, v62, v68
	v_lshlrev_b32_e32 v68, 16, v81
	v_mul_f32_e32 v66, v66, v67
	v_mul_f32_e32 v64, v64, v68
	v_and_b32_e32 v68, 0xffff0000, v81
	v_mul_f32_e32 v63, v199, v56
	v_mul_f32_e32 v66, v66, v68
	s_waitcnt vmcnt(7)
	v_lshlrev_b32_e32 v68, 16, v82
	v_mul_f32_e32 v63, v63, v69
	v_mul_f32_e32 v65, v193, v56
	v_mul_f32_e32 v68, v61, v68
	v_and_b32_e32 v61, 0xffff0000, v82
	v_mul_f32_e32 v65, v65, v70
	v_mul_f32_e32 v67, v191, v56
	v_mul_f32_e32 v63, v63, v61
	v_lshlrev_b32_e32 v61, 16, v83
	v_mul_f32_e32 v67, v67, v71
	v_mul_f32_e32 v65, v65, v61
	v_and_b32_e32 v61, 0xffff0000, v83
	v_mul_f32_e32 v67, v67, v61
	v_cvt_pk_bf16_f32 v60, v60, v62
	v_cvt_pk_bf16_f32 v61, v64, v66
	v_cvt_pk_bf16_f32 v62, v68, v63
	v_cvt_pk_bf16_f32 v63, v65, v67
	v_or_b32_e32 v64, 64, v58
	v_permlane32_swap_b32_e32 v60, v62
	v_permlane32_swap_b32_e32 v61, v63
	global_store_dwordx4 v64, v[60:63], s[4:5] offset:32
	global_load_dwordx2 v[76:77], v59, s[4:5] offset:192
	global_load_dwordx2 v[78:79], v59, s[4:5] offset:208
	global_load_dwordx2 v[80:81], v59, s[4:5] offset:224
	global_load_dwordx2 v[82:83], v59, s[4:5] offset:240
	ds_read_b128 v[60:63], v57 offset:256
	ds_read_b128 v[64:67], v57 offset:288
	v_mul_f32_e32 v68, v188, v56
	v_mul_f32_e32 v44, v44, v56
	v_mul_f32_e32 v42, v42, v56
	s_waitcnt lgkmcnt(1)
	v_mul_f32_e32 v60, v68, v60
	v_mul_f32_e32 v68, v189, v56
	s_waitcnt lgkmcnt(0)
	v_mul_f32_e32 v64, v68, v64
	v_mul_f32_e32 v68, v186, v56
	v_mul_f32_e32 v61, v68, v61
	v_mul_f32_e32 v68, v187, v56
	v_mul_f32_e32 v65, v68, v65
	v_mul_f32_e32 v68, v184, v56
	v_mul_f32_e32 v62, v68, v62
	v_mul_f32_e32 v68, v185, v56
	v_mul_f32_e32 v66, v68, v66
	v_mul_f32_e32 v68, v182, v56
	v_mul_f32_e32 v63, v68, v63
	v_mul_f32_e32 v68, v183, v56
	v_mul_f32_e32 v67, v68, v67
	s_waitcnt vmcnt(9)
	v_lshlrev_b32_e32 v68, 16, v72
	v_mul_f32_e32 v60, v60, v68
	v_and_b32_e32 v68, 0xffff0000, v72
	v_mul_f32_e32 v61, v61, v68
	v_lshlrev_b32_e32 v68, 16, v73
	v_mul_f32_e32 v62, v62, v68
	v_and_b32_e32 v68, 0xffff0000, v73
	v_mul_f32_e32 v63, v63, v68
	s_waitcnt vmcnt(8)
	v_lshlrev_b32_e32 v68, 16, v74
	v_mul_f32_e32 v64, v64, v68
	v_and_b32_e32 v68, 0xffff0000, v74
	v_mul_f32_e32 v65, v65, v68
	v_lshlrev_b32_e32 v68, 16, v75
	v_mul_f32_e32 v66, v66, v68
	v_and_b32_e32 v68, 0xffff0000, v75
	v_mul_f32_e32 v67, v67, v68
	v_cvt_pk_bf16_f32 v60, v60, v61
	v_cvt_pk_bf16_f32 v61, v62, v63
	v_cvt_pk_bf16_f32 v62, v64, v65
	v_cvt_pk_bf16_f32 v63, v66, v67
	ds_read_b128 v[64:67], v57 offset:320
	ds_read_b128 v[68:71], v57 offset:352
	v_permlane32_swap_b32_e32 v60, v62
	v_permlane32_swap_b32_e32 v61, v63
	global_store_dwordx4 v58, v[60:63], s[4:5] offset:128
	v_mul_f32_e32 v40, v40, v56
	v_mul_f32_e32 v47, v47, v56
	v_mul_f32_e32 v60, v180, v56
	v_mul_f32_e32 v61, v181, v56
	s_waitcnt lgkmcnt(1)
	v_mul_f32_e32 v60, v60, v64
	s_waitcnt lgkmcnt(0)
	v_mul_f32_e32 v61, v61, v68
	v_mul_f32_e32 v62, v178, v56
	s_waitcnt vmcnt(8)
	v_lshlrev_b32_e32 v68, 16, v84
	v_mul_f32_e32 v62, v62, v65
	v_mul_f32_e32 v64, v173, v56
	v_mul_f32_e32 v60, v60, v68
	v_and_b32_e32 v68, 0xffff0000, v84
	v_mul_f32_e32 v64, v64, v66
	v_mul_f32_e32 v66, v171, v56
	v_mul_f32_e32 v62, v62, v68
	v_lshlrev_b32_e32 v68, 16, v85
	v_mul_f32_e32 v66, v66, v67
	v_mul_f32_e32 v64, v64, v68
	v_and_b32_e32 v68, 0xffff0000, v85
	v_mul_f32_e32 v63, v179, v56
	v_mul_f32_e32 v66, v66, v68
	s_waitcnt vmcnt(7)
	v_lshlrev_b32_e32 v68, 16, v86
	v_mul_f32_e32 v63, v63, v69
	v_mul_f32_e32 v65, v177, v56
	v_mul_f32_e32 v68, v61, v68
	v_and_b32_e32 v61, 0xffff0000, v86
	v_mul_f32_e32 v65, v65, v70
	v_mul_f32_e32 v67, v172, v56
	v_mul_f32_e32 v63, v63, v61
	v_lshlrev_b32_e32 v61, 16, v87
	v_mul_f32_e32 v67, v67, v71
	v_mul_f32_e32 v65, v65, v61
	v_and_b32_e32 v61, 0xffff0000, v87
	v_mul_f32_e32 v67, v67, v61
	v_cvt_pk_bf16_f32 v60, v60, v62
	v_cvt_pk_bf16_f32 v61, v64, v66
	v_cvt_pk_bf16_f32 v62, v68, v63
	v_cvt_pk_bf16_f32 v63, v65, v67
	v_or_b32_e32 v64, 0x80, v58
	v_permlane32_swap_b32_e32 v60, v62
	v_permlane32_swap_b32_e32 v61, v63
	global_store_dwordx4 v64, v[60:63], s[4:5] offset:32
	global_load_dwordx2 v[72:73], v59, s[4:5] offset:256
	global_load_dwordx2 v[74:75], v59, s[4:5] offset:272
	global_load_dwordx2 v[84:85], v59, s[4:5] offset:288
	global_load_dwordx2 v[86:87], v59, s[4:5] offset:304
	ds_read_b128 v[60:63], v57 offset:384
	ds_read_b128 v[64:67], v57 offset:416
	v_mul_f32_e32 v68, v163, v56
	v_mul_f32_e32 v45, v45, v56
	v_mul_f32_e32 v43, v43, v56
	s_waitcnt lgkmcnt(1)
	v_mul_f32_e32 v60, v68, v60
	v_mul_f32_e32 v68, v170, v56
	s_waitcnt lgkmcnt(0)
	v_mul_f32_e32 v64, v68, v64
	v_mul_f32_e32 v68, v160, v56
	v_mul_f32_e32 v61, v68, v61
	v_mul_f32_e32 v68, v162, v56
	v_mul_f32_e32 v65, v68, v65
	v_mul_f32_e32 v68, v158, v56
	v_mul_f32_e32 v62, v68, v62
	v_mul_f32_e32 v68, v159, v56
	v_mul_f32_e32 v66, v68, v66
	v_mul_f32_e32 v68, v156, v56
	v_mul_f32_e32 v63, v68, v63
	v_mul_f32_e32 v68, v157, v56
	v_mul_f32_e32 v67, v68, v67
	s_waitcnt vmcnt(9)
	v_lshlrev_b32_e32 v68, 16, v76
	v_mul_f32_e32 v60, v60, v68
	v_and_b32_e32 v68, 0xffff0000, v76
	v_mul_f32_e32 v61, v61, v68
	v_lshlrev_b32_e32 v68, 16, v77
	v_mul_f32_e32 v62, v62, v68
	v_and_b32_e32 v68, 0xffff0000, v77
	v_mul_f32_e32 v63, v63, v68
	s_waitcnt vmcnt(8)
	v_lshlrev_b32_e32 v68, 16, v78
	v_mul_f32_e32 v64, v64, v68
	v_and_b32_e32 v68, 0xffff0000, v78
	v_mul_f32_e32 v65, v65, v68
	v_lshlrev_b32_e32 v68, 16, v79
	v_mul_f32_e32 v66, v66, v68
	v_and_b32_e32 v68, 0xffff0000, v79
	v_mul_f32_e32 v67, v67, v68
	v_cvt_pk_bf16_f32 v60, v60, v61
	v_cvt_pk_bf16_f32 v61, v62, v63
	v_cvt_pk_bf16_f32 v62, v64, v65
	v_cvt_pk_bf16_f32 v63, v66, v67
	ds_read_b128 v[64:67], v57 offset:448
	ds_read_b128 v[68:71], v57 offset:480
	v_permlane32_swap_b32_e32 v60, v62
	v_permlane32_swap_b32_e32 v61, v63
	global_store_dwordx4 v58, v[60:63], s[4:5] offset:192
	v_mul_f32_e32 v41, v41, v56
	v_mul_f32_e32 v38, v38, v56
	v_mul_f32_e32 v60, v126, v56
	v_mul_f32_e32 v61, v127, v56
	s_waitcnt lgkmcnt(1)
	v_mul_f32_e32 v60, v60, v64
	s_waitcnt lgkmcnt(0)
	v_mul_f32_e32 v61, v61, v68
	v_mul_f32_e32 v62, v124, v56
	s_waitcnt vmcnt(8)
	v_lshlrev_b32_e32 v68, 16, v80
	v_mul_f32_e32 v62, v62, v65
	v_mul_f32_e32 v64, v122, v56
	v_mul_f32_e32 v60, v60, v68
	v_and_b32_e32 v68, 0xffff0000, v80
	v_mul_f32_e32 v64, v64, v66
	v_mul_f32_e32 v66, v120, v56
	v_mul_f32_e32 v62, v62, v68
	v_lshlrev_b32_e32 v68, 16, v81
	v_mul_f32_e32 v66, v66, v67
	v_mul_f32_e32 v64, v64, v68
	v_and_b32_e32 v68, 0xffff0000, v81
	v_mul_f32_e32 v63, v125, v56
	v_mul_f32_e32 v66, v66, v68
	s_waitcnt vmcnt(7)
	v_lshlrev_b32_e32 v68, 16, v82
	v_mul_f32_e32 v63, v63, v69
	v_mul_f32_e32 v65, v123, v56
	v_mul_f32_e32 v68, v61, v68
	v_and_b32_e32 v61, 0xffff0000, v82
	v_mul_f32_e32 v65, v65, v70
	v_mul_f32_e32 v67, v121, v56
	v_mul_f32_e32 v63, v63, v61
	v_lshlrev_b32_e32 v61, 16, v83
	v_mul_f32_e32 v67, v67, v71
	v_mul_f32_e32 v65, v65, v61
	v_and_b32_e32 v61, 0xffff0000, v83
	v_mul_f32_e32 v67, v67, v61
	v_cvt_pk_bf16_f32 v60, v60, v62
	v_cvt_pk_bf16_f32 v61, v64, v66
	v_cvt_pk_bf16_f32 v62, v68, v63
	v_cvt_pk_bf16_f32 v63, v65, v67
	v_or_b32_e32 v64, 0xc0, v58
	v_permlane32_swap_b32_e32 v60, v62
	v_permlane32_swap_b32_e32 v61, v63
	global_store_dwordx4 v64, v[60:63], s[4:5] offset:32
	global_load_dwordx2 v[76:77], v59, s[4:5] offset:320
	global_load_dwordx2 v[78:79], v59, s[4:5] offset:336
	global_load_dwordx2 v[80:81], v59, s[4:5] offset:352
	global_load_dwordx2 v[82:83], v59, s[4:5] offset:368
	ds_read_b128 v[60:63], v57 offset:512
	ds_read_b128 v[64:67], v57 offset:544
	v_mul_f32_e32 v68, v118, v56
	v_mul_f32_e32 v36, v36, v56
	v_mul_f32_e32 v34, v34, v56
	s_waitcnt lgkmcnt(1)
	v_mul_f32_e32 v60, v68, v60
	v_mul_f32_e32 v68, v119, v56
	s_waitcnt lgkmcnt(0)
	v_mul_f32_e32 v64, v68, v64
	v_mul_f32_e32 v68, v116, v56
	v_mul_f32_e32 v61, v68, v61
	v_mul_f32_e32 v68, v117, v56
	v_mul_f32_e32 v65, v68, v65
	v_mul_f32_e32 v68, v114, v56
	v_mul_f32_e32 v62, v68, v62
	v_mul_f32_e32 v68, v115, v56
	v_mul_f32_e32 v66, v68, v66
	v_mul_f32_e32 v68, v112, v56
	v_mul_f32_e32 v63, v68, v63
	v_mul_f32_e32 v68, v113, v56
	v_mul_f32_e32 v67, v68, v67
	s_waitcnt vmcnt(9)
	v_lshlrev_b32_e32 v68, 16, v72
	v_mul_f32_e32 v60, v60, v68
	v_and_b32_e32 v68, 0xffff0000, v72
	v_mul_f32_e32 v61, v61, v68
	v_lshlrev_b32_e32 v68, 16, v73
	v_mul_f32_e32 v62, v62, v68
	v_and_b32_e32 v68, 0xffff0000, v73
	v_mul_f32_e32 v63, v63, v68
	s_waitcnt vmcnt(8)
	v_lshlrev_b32_e32 v68, 16, v74
	v_mul_f32_e32 v64, v64, v68
	v_and_b32_e32 v68, 0xffff0000, v74
	v_mul_f32_e32 v65, v65, v68
	v_lshlrev_b32_e32 v68, 16, v75
	v_mul_f32_e32 v66, v66, v68
	v_and_b32_e32 v68, 0xffff0000, v75
	v_mul_f32_e32 v67, v67, v68
	v_cvt_pk_bf16_f32 v60, v60, v61
	v_cvt_pk_bf16_f32 v61, v62, v63
	v_cvt_pk_bf16_f32 v62, v64, v65
	v_cvt_pk_bf16_f32 v63, v66, v67
	ds_read_b128 v[64:67], v57 offset:576
	ds_read_b128 v[68:71], v57 offset:608
	v_permlane32_swap_b32_e32 v60, v62
	v_permlane32_swap_b32_e32 v61, v63
	global_store_dwordx4 v58, v[60:63], s[4:5] offset:256
	s_waitcnt lgkmcnt(1)
	v_mul_f32_e32 v54, v54, v64
	v_mul_f32_e32 v52, v52, v65
	s_waitcnt vmcnt(8)
	v_lshlrev_b32_e32 v60, 16, v84
	v_mul_f32_e32 v54, v54, v60
	v_and_b32_e32 v60, 0xffff0000, v84
	v_mul_f32_e32 v50, v50, v66
	v_mul_f32_e32 v52, v52, v60
	v_lshlrev_b32_e32 v60, 16, v85
	v_mul_f32_e32 v48, v48, v67
	v_mul_f32_e32 v50, v50, v60
	v_and_b32_e32 v60, 0xffff0000, v85
	s_waitcnt lgkmcnt(0)
	v_mul_f32_e32 v55, v55, v68
	v_mul_f32_e32 v60, v48, v60
	s_waitcnt vmcnt(7)
	v_lshlrev_b32_e32 v48, 16, v86
	v_mul_f32_e32 v53, v53, v69
	v_mul_f32_e32 v55, v55, v48
	v_and_b32_e32 v48, 0xffff0000, v86
	v_mul_f32_e32 v51, v51, v70
	v_mul_f32_e32 v53, v53, v48
	v_lshlrev_b32_e32 v48, 16, v87
	v_mul_f32_e32 v49, v49, v71
	v_mul_f32_e32 v51, v51, v48
	v_and_b32_e32 v48, 0xffff0000, v87
	v_mul_f32_e32 v61, v49, v48
	v_cvt_pk_bf16_f32 v48, v54, v52
	v_cvt_pk_bf16_f32 v49, v50, v60
	v_cvt_pk_bf16_f32 v50, v55, v53
	v_cvt_pk_bf16_f32 v51, v51, v61
	v_or_b32_e32 v52, 0x100, v58
	v_permlane32_swap_b32_e32 v48, v50
	v_permlane32_swap_b32_e32 v49, v51
	global_store_dwordx4 v52, v[48:51], s[4:5] offset:32
	global_load_dwordx2 v[60:61], v59, s[4:5] offset:384
	global_load_dwordx2 v[62:63], v59, s[4:5] offset:400
	global_load_dwordx2 v[64:65], v59, s[4:5] offset:416
	global_load_dwordx2 v[66:67], v59, s[4:5] offset:432
	ds_read_b128 v[48:51], v57 offset:640
	ds_read_b128 v[52:55], v57 offset:672
	v_mul_f32_e32 v32, v32, v56
	v_mul_f32_e32 v39, v39, v56
	v_mul_f32_e32 v37, v37, v56
	s_waitcnt lgkmcnt(1)
	v_mul_f32_e32 v46, v46, v48
	s_waitcnt vmcnt(9)
	v_lshlrev_b32_e32 v48, 16, v76
	v_mul_f32_e32 v44, v44, v49
	v_mul_f32_e32 v46, v46, v48
	v_and_b32_e32 v48, 0xffff0000, v76
	v_mul_f32_e32 v42, v42, v50
	v_mul_f32_e32 v44, v44, v48
	v_lshlrev_b32_e32 v48, 16, v77
	v_mul_f32_e32 v40, v40, v51
	v_mul_f32_e32 v42, v42, v48
	v_and_b32_e32 v48, 0xffff0000, v77
	s_waitcnt lgkmcnt(0)
	v_mul_f32_e32 v47, v47, v52
	v_mul_f32_e32 v48, v40, v48
	s_waitcnt vmcnt(8)
	v_lshlrev_b32_e32 v40, 16, v78
	v_mul_f32_e32 v45, v45, v53
	v_mul_f32_e32 v47, v47, v40
	v_and_b32_e32 v40, 0xffff0000, v78
	v_mul_f32_e32 v43, v43, v54
	v_mul_f32_e32 v45, v45, v40
	v_lshlrev_b32_e32 v40, 16, v79
	v_mul_f32_e32 v41, v41, v55
	v_mul_f32_e32 v43, v43, v40
	v_and_b32_e32 v40, 0xffff0000, v79
	v_mul_f32_e32 v49, v41, v40
	v_cvt_pk_bf16_f32 v40, v46, v44
	v_cvt_pk_bf16_f32 v41, v42, v48
	v_cvt_pk_bf16_f32 v42, v47, v45
	v_cvt_pk_bf16_f32 v43, v43, v49
	ds_read_b128 v[44:47], v57 offset:704
	ds_read_b128 v[48:51], v57 offset:736
	v_permlane32_swap_b32_e32 v40, v42
	v_permlane32_swap_b32_e32 v41, v43
	global_store_dwordx4 v58, v[40:43], s[4:5] offset:320
	s_waitcnt lgkmcnt(1)
	v_mul_f32_e32 v38, v38, v44
	v_mul_f32_e32 v36, v36, v45
	s_waitcnt vmcnt(8)
	v_lshlrev_b32_e32 v40, 16, v80
	v_mul_f32_e32 v38, v38, v40
	v_and_b32_e32 v40, 0xffff0000, v80
	v_mul_f32_e32 v34, v34, v46
	v_mul_f32_e32 v36, v36, v40
	v_lshlrev_b32_e32 v40, 16, v81
	v_mul_f32_e32 v32, v32, v47
	v_mul_f32_e32 v34, v34, v40
	v_and_b32_e32 v40, 0xffff0000, v81
	s_waitcnt lgkmcnt(0)
	v_mul_f32_e32 v39, v39, v48
	v_mul_f32_e32 v40, v32, v40
	s_waitcnt vmcnt(7)
	v_lshlrev_b32_e32 v32, 16, v82
	v_mul_f32_e32 v37, v37, v49
	v_mul_f32_e32 v35, v35, v56
	v_mul_f32_e32 v39, v39, v32
	v_and_b32_e32 v32, 0xffff0000, v82
	v_mul_f32_e32 v35, v35, v50
	v_mul_f32_e32 v33, v33, v56
	v_mul_f32_e32 v37, v37, v32
	v_lshlrev_b32_e32 v32, 16, v83
	v_mul_f32_e32 v33, v33, v51
	v_mul_f32_e32 v35, v35, v32
	v_and_b32_e32 v32, 0xffff0000, v83
	v_mul_f32_e32 v41, v33, v32
	v_cvt_pk_bf16_f32 v32, v38, v36
	v_cvt_pk_bf16_f32 v33, v34, v40
	v_cvt_pk_bf16_f32 v34, v39, v37
	v_cvt_pk_bf16_f32 v35, v35, v41
	v_or_b32_e32 v36, 0x140, v58
	v_permlane32_swap_b32_e32 v32, v34
	v_permlane32_swap_b32_e32 v33, v35
	global_store_dwordx4 v36, v[32:35], s[4:5] offset:32
	global_load_dwordx2 v[40:41], v59, s[4:5] offset:448
	global_load_dwordx2 v[42:43], v59, s[4:5] offset:464
	global_load_dwordx2 v[44:45], v59, s[4:5] offset:480
	global_load_dwordx2 v[46:47], v59, s[4:5] offset:496
	ds_read_b128 v[32:35], v57 offset:768
	ds_read_b128 v[36:39], v57 offset:800
	v_mul_f32_e32 v30, v30, v56
	v_mul_f32_e32 v28, v28, v56
	v_mul_f32_e32 v26, v26, v56
	s_waitcnt lgkmcnt(1)
	v_mul_f32_e32 v30, v30, v32
	s_waitcnt vmcnt(9)
	v_lshlrev_b32_e32 v32, 16, v60
	v_mul_f32_e32 v28, v28, v33
	v_mul_f32_e32 v30, v30, v32
	v_and_b32_e32 v32, 0xffff0000, v60
	v_mul_f32_e32 v26, v26, v34
	v_mul_f32_e32 v24, v24, v56
	v_mul_f32_e32 v28, v28, v32
	v_lshlrev_b32_e32 v32, 16, v61
	v_mul_f32_e32 v31, v31, v56
	v_mul_f32_e32 v24, v24, v35
	v_mul_f32_e32 v26, v26, v32
	v_and_b32_e32 v32, 0xffff0000, v61
	s_waitcnt lgkmcnt(0)
	v_mul_f32_e32 v31, v31, v36
	v_mul_f32_e32 v29, v29, v56
	v_mul_f32_e32 v32, v24, v32
	s_waitcnt vmcnt(8)
	v_lshlrev_b32_e32 v24, 16, v62
	v_mul_f32_e32 v29, v29, v37
	v_mul_f32_e32 v27, v27, v56
	v_mul_f32_e32 v31, v31, v24
	v_and_b32_e32 v24, 0xffff0000, v62
	v_mul_f32_e32 v27, v27, v38
	v_mul_f32_e32 v25, v25, v56
	v_mul_f32_e32 v29, v29, v24
	v_lshlrev_b32_e32 v24, 16, v63
	v_mul_f32_e32 v25, v25, v39
	v_mul_f32_e32 v27, v27, v24
	v_and_b32_e32 v24, 0xffff0000, v63
	v_mul_f32_e32 v33, v25, v24
	v_cvt_pk_bf16_f32 v24, v30, v28
	v_cvt_pk_bf16_f32 v25, v26, v32
	v_cvt_pk_bf16_f32 v26, v31, v29
	v_cvt_pk_bf16_f32 v27, v27, v33
	ds_read_b128 v[28:31], v57 offset:832
	ds_read_b128 v[32:35], v57 offset:864
	v_permlane32_swap_b32_e32 v24, v26
	v_permlane32_swap_b32_e32 v25, v27
	v_mul_f32_e32 v22, v22, v56
	global_store_dwordx4 v58, v[24:27], s[4:5] offset:384
	s_waitcnt lgkmcnt(1)
	v_mul_f32_e32 v22, v22, v28
	v_mul_f32_e32 v20, v20, v56
	s_waitcnt vmcnt(8)
	v_lshlrev_b32_e32 v24, 16, v64
	v_mul_f32_e32 v20, v20, v29
	v_mul_f32_e32 v18, v18, v56
	v_mul_f32_e32 v22, v22, v24
	v_and_b32_e32 v24, 0xffff0000, v64
	v_mul_f32_e32 v18, v18, v30
	v_mul_f32_e32 v16, v16, v56
	v_mul_f32_e32 v20, v20, v24
	v_lshlrev_b32_e32 v24, 16, v65
	v_mul_f32_e32 v23, v23, v56
	v_mul_f32_e32 v16, v16, v31
	v_mul_f32_e32 v18, v18, v24
	v_and_b32_e32 v24, 0xffff0000, v65
	s_waitcnt lgkmcnt(0)
	v_mul_f32_e32 v23, v23, v32
	v_mul_f32_e32 v21, v21, v56
	v_mul_f32_e32 v24, v16, v24
	s_waitcnt vmcnt(7)
	v_lshlrev_b32_e32 v16, 16, v66
	v_mul_f32_e32 v21, v21, v33
	v_mul_f32_e32 v19, v19, v56
	v_mul_f32_e32 v23, v23, v16
	v_and_b32_e32 v16, 0xffff0000, v66
	v_mul_f32_e32 v19, v19, v34
	v_mul_f32_e32 v17, v17, v56
	v_mul_f32_e32 v21, v21, v16
	v_lshlrev_b32_e32 v16, 16, v67
	v_mul_f32_e32 v17, v17, v35
	v_mul_f32_e32 v19, v19, v16
	v_and_b32_e32 v16, 0xffff0000, v67
	v_mul_f32_e32 v25, v17, v16
	v_cvt_pk_bf16_f32 v16, v22, v20
	v_cvt_pk_bf16_f32 v17, v18, v24
	v_cvt_pk_bf16_f32 v18, v23, v21
	v_cvt_pk_bf16_f32 v19, v19, v25
	v_or_b32_e32 v20, 0x180, v58
	v_permlane32_swap_b32_e32 v16, v18
	v_permlane32_swap_b32_e32 v17, v19
	global_store_dwordx4 v20, v[16:19], s[4:5] offset:32
	ds_read_b128 v[16:19], v57 offset:896
	ds_read_b128 v[20:23], v57 offset:928
	v_mul_f32_e32 v14, v14, v56
	v_mul_f32_e32 v12, v12, v56
	v_mul_f32_e32 v10, v10, v56
	s_waitcnt lgkmcnt(1)
	v_mul_f32_e32 v14, v14, v16
	s_waitcnt vmcnt(5)
	v_lshlrev_b32_e32 v16, 16, v40
	v_mul_f32_e32 v12, v12, v17
	v_mul_f32_e32 v14, v14, v16
	v_and_b32_e32 v16, 0xffff0000, v40
	v_mul_f32_e32 v10, v10, v18
	v_mul_f32_e32 v8, v8, v56
	v_mul_f32_e32 v12, v12, v16
	v_lshlrev_b32_e32 v16, 16, v41
	v_mul_f32_e32 v15, v15, v56
	v_mul_f32_e32 v8, v8, v19
	v_mul_f32_e32 v10, v10, v16
	v_and_b32_e32 v16, 0xffff0000, v41
	s_waitcnt lgkmcnt(0)
	v_mul_f32_e32 v15, v15, v20
	v_mul_f32_e32 v13, v13, v56
	v_mul_f32_e32 v16, v8, v16
	s_waitcnt vmcnt(4)
	v_lshlrev_b32_e32 v8, 16, v42
	v_mul_f32_e32 v13, v13, v21
	v_mul_f32_e32 v11, v11, v56
	v_mul_f32_e32 v15, v15, v8
	v_and_b32_e32 v8, 0xffff0000, v42
	v_mul_f32_e32 v11, v11, v22
	v_mul_f32_e32 v9, v9, v56
	v_mul_f32_e32 v13, v13, v8
	v_lshlrev_b32_e32 v8, 16, v43
	v_mul_f32_e32 v9, v9, v23
	v_mul_f32_e32 v11, v11, v8
	v_and_b32_e32 v8, 0xffff0000, v43
	v_mul_f32_e32 v17, v9, v8
	v_cvt_pk_bf16_f32 v8, v14, v12
	v_cvt_pk_bf16_f32 v9, v10, v16
	v_cvt_pk_bf16_f32 v10, v15, v13
	v_cvt_pk_bf16_f32 v11, v11, v17
	ds_read_b128 v[12:15], v57 offset:960
	ds_read_b128 v[16:19], v57 offset:992
	v_permlane32_swap_b32_e32 v8, v10
	v_permlane32_swap_b32_e32 v9, v11
	v_mul_f32_e32 v6, v6, v56
	global_store_dwordx4 v58, v[8:11], s[4:5] offset:448
	s_waitcnt lgkmcnt(1)
	v_mul_f32_e32 v6, v6, v12
	v_mul_f32_e32 v4, v4, v56
	s_waitcnt vmcnt(4)
	v_lshlrev_b32_e32 v8, 16, v44
	v_mul_f32_e32 v4, v4, v13
	v_mul_f32_e32 v2, v2, v56
	v_mul_f32_e32 v6, v6, v8
	v_and_b32_e32 v8, 0xffff0000, v44
	v_mul_f32_e32 v2, v2, v14
	v_mul_f32_e32 v0, v0, v56
	v_mul_f32_e32 v4, v4, v8
	v_lshlrev_b32_e32 v8, 16, v45
	v_mul_f32_e32 v7, v7, v56
	v_mul_f32_e32 v0, v0, v15
	v_mul_f32_e32 v2, v2, v8
	v_and_b32_e32 v8, 0xffff0000, v45
	s_waitcnt lgkmcnt(0)
	v_mul_f32_e32 v7, v7, v16
	v_mul_f32_e32 v5, v5, v56
	v_mul_f32_e32 v8, v0, v8
	s_waitcnt vmcnt(3)
	v_lshlrev_b32_e32 v0, 16, v46
	v_mul_f32_e32 v5, v5, v17
	v_mul_f32_e32 v3, v3, v56
	v_mul_f32_e32 v7, v7, v0
	v_and_b32_e32 v0, 0xffff0000, v46
	v_mul_f32_e32 v3, v3, v18
	v_mul_f32_e32 v1, v1, v56
	v_mul_f32_e32 v5, v5, v0
	v_lshlrev_b32_e32 v0, 16, v47
	v_mul_f32_e32 v1, v1, v19
	v_mul_f32_e32 v3, v3, v0
	v_and_b32_e32 v0, 0xffff0000, v47
	v_mul_f32_e32 v9, v1, v0
	v_cvt_pk_bf16_f32 v0, v6, v4
	v_cvt_pk_bf16_f32 v1, v2, v8
	v_cvt_pk_bf16_f32 v2, v7, v5
	v_cvt_pk_bf16_f32 v3, v3, v9
	v_readlane_b32 s2, v255, 38
	v_permlane32_swap_b32_e32 v0, v2
	v_permlane32_swap_b32_e32 v1, v3
	v_or_b32_e32 v4, 0x1c0, v58
	s_cmp_lg_u32 s10, s2
	s_mov_b32 s2, s10
	global_store_dwordx4 v4, v[0:3], s[4:5] offset:32
	s_cbranch_scc0 .LBB0_541
.LBB0_515:
	s_add_i32 s17, s2, 1
	s_mov_b64 s[4:5], exec
	v_readlane_b32 s6, v255, 29
	v_readlane_b32 s7, v255, 30
	s_and_b64 s[6:7], s[4:5], s[6:7]
	s_mov_b64 exec, s[6:7]
	s_cbranch_execz .LBB0_517
	v_readlane_b32 s3, v255, 37
	s_cmp_lt_u32 s17, s3
	s_cselect_b32 s3, s17, s2
	s_lshr_b32 s6, s3, 1
	s_mul_i32 s6, s6, s15
	v_readlane_b32 s7, v255, 16
	s_add_i32 s12, s6, s7
	s_lshl_b32 s6, s12, 7
	s_and_b32 s6, s6, 0xfffff000
	s_ashr_i32 s7, s6, 31
	s_mul_i32 s9, s6, 0x6800
	s_mul_hi_i32 s8, s6, 0x6800
	s_add_u32 s9, s80, s9
	s_addc_u32 s8, s85, s8
	s_bfe_u32 s10, s12, 0x20003
	s_lshl_b32 s13, s10, 8
	s_lshl_b32 s10, s10, 9
	s_add_u32 s9, s9, s10
	s_addc_u32 s10, s8, 0
	s_add_u32 s8, s9, 0x800
	s_addc_u32 s9, s10, 0
	s_lshl_b64 s[10:11], s[6:7], 11
	v_readlane_b32 s14, v255, 25
	s_add_u32 s7, s14, s10
	v_readlane_b32 s16, v255, 26
	s_addc_u32 s10, s16, s11
	s_add_u32 s7, s7, s13
	s_addc_u32 s11, s10, 0
	s_add_u32 s10, s7, 0x400
	s_addc_u32 s11, s11, 0
	s_lshl_b32 s7, s12, 8
	s_and_b32 s7, s7, 0x700
	s_and_b32 s3, s3, 1
	s_xor_b32 s12, s7, 0xf00
	s_cmp_eq_u32 s3, 0
	s_cselect_b32 s3, s12, s7
	s_or_b32 s6, s3, s6
	s_ashr_i32 s7, s6, 31
	s_lshl_b64 s[6:7], s[6:7], 11
	s_add_u32 s3, s14, s6
	s_addc_u32 s7, s16, s7
	s_add_u32 s6, s3, s13
	v_readlane_b32 s12, v255, 31
	s_addc_u32 s7, s7, 0
	v_readlane_b32 s13, v255, 32
	v_mov_b64_e32 v[2:3], s[6:7]
	s_nop 0
	v_mov_b64_e32 v[0:1], s[12:13]
	ds_write_b64 v0, v[2:3]
	s_waitcnt lgkmcnt(0)
	v_mov_b64_e32 v[0:1], s[0:1]
	v_mov_b64_e32 v[2:3], s[10:11]
	ds_write_b64 v0, v[2:3]
	s_waitcnt lgkmcnt(0)
	v_mov_b64_e32 v[0:1], s[70:71]
	v_mov_b64_e32 v[2:3], s[8:9]
	ds_write_b64 v0, v[2:3]
	s_waitcnt lgkmcnt(0)

.LBB0_551:
	v_add_f32_e32 v162, v144, v145
	v_fmac_f32_e32 v162, v178, v160
	v_mul_u32_u24_e32 v160, 0x6800, v176
	ds_read_b64_tr_b16 v[144:145], v177 offset:0x8000
	ds_read_b64_tr_b16 v[146:147], v177 offset:0x9000
	ds_read_b64_tr_b16 v[148:149], v177 offset:0xa000
	ds_read_b64_tr_b16 v[150:151], v177 offset:0xb000
	ds_read_b64_tr_b16 v[152:153], v177 offset:0xc000
	ds_read_b64_tr_b16 v[154:155], v177 offset:0xd000
	ds_read_b64_tr_b16 v[156:157], v177 offset:0xe000
	ds_read_b64_tr_b16 v[158:159], v177 offset:0xf000
	ds_read_b64_tr_b16 v[166:167], v177 offset:0x8200
	ds_read_b64_tr_b16 v[168:169], v177 offset:0x9200
	ds_read_b64_tr_b16 v[178:179], v177 offset:0xa200
	ds_read_b64_tr_b16 v[180:181], v177 offset:0xb200
	ds_read_b64_tr_b16 v[182:183], v177 offset:0xc200
	ds_read_b64_tr_b16 v[184:185], v177 offset:0xd200
	ds_read_b64_tr_b16 v[186:187], v177 offset:0xe200
	ds_read_b64_tr_b16 v[188:189], v177 offset:0xf200
	s_waitcnt lgkmcnt(8)
	s_nop 0
	v_mfma_f32_32x32x16_bf16 v[112:127], v[144:147], v[128:131], v[112:127]
	v_mfma_f32_32x32x16_bf16 v[112:127], v[148:151], v[132:135], v[112:127]
	v_mfma_f32_32x32x16_bf16 v[112:127], v[152:155], v[136:139], v[112:127]
	v_mfma_f32_32x32x16_bf16 v[112:127], v[156:159], v[140:143], v[112:127]
	ds_read_b64_tr_b16 v[144:145], v177 offset:0x8400
	ds_read_b64_tr_b16 v[146:147], v177 offset:0x9400
	ds_read_b64_tr_b16 v[148:149], v177 offset:0xa400
	ds_read_b64_tr_b16 v[150:151], v177 offset:0xb400
	ds_read_b64_tr_b16 v[152:153], v177 offset:0xc400
	ds_read_b64_tr_b16 v[154:155], v177 offset:0xd400
	ds_read_b64_tr_b16 v[156:157], v177 offset:0xe400
	ds_read_b64_tr_b16 v[158:159], v177 offset:0xf400
	s_waitcnt lgkmcnt(8)
	v_mfma_f32_32x32x16_bf16 v[96:111], v[166:169], v[128:131], v[96:111]
	v_mfma_f32_32x32x16_bf16 v[96:111], v[178:181], v[132:135], v[96:111]
	v_mfma_f32_32x32x16_bf16 v[96:111], v[182:185], v[136:139], v[96:111]
	v_mfma_f32_32x32x16_bf16 v[96:111], v[186:189], v[140:143], v[96:111]
	ds_read_b64_tr_b16 v[166:167], v177 offset:0x8600
	ds_read_b64_tr_b16 v[168:169], v177 offset:0x9600
	ds_read_b64_tr_b16 v[178:179], v177 offset:0xa600
	ds_read_b64_tr_b16 v[180:181], v177 offset:0xb600
	ds_read_b64_tr_b16 v[182:183], v177 offset:0xc600
	ds_read_b64_tr_b16 v[184:185], v177 offset:0xd600
	ds_read_b64_tr_b16 v[186:187], v177 offset:0xe600
	ds_read_b64_tr_b16 v[188:189], v177 offset:0xf600
	s_waitcnt lgkmcnt(8)
	v_mfma_f32_32x32x16_bf16 v[80:95], v[144:147], v[128:131], v[80:95]
	v_mfma_f32_32x32x16_bf16 v[80:95], v[148:151], v[132:135], v[80:95]
	v_mfma_f32_32x32x16_bf16 v[80:95], v[152:155], v[136:139], v[80:95]
	v_mfma_f32_32x32x16_bf16 v[80:95], v[156:159], v[140:143], v[80:95]
	ds_read_b64_tr_b16 v[144:145], v177 offset:0x8800
	ds_read_b64_tr_b16 v[146:147], v177 offset:0x9800
	ds_read_b64_tr_b16 v[148:149], v177 offset:0xa800
	ds_read_b64_tr_b16 v[150:151], v177 offset:0xb800
	ds_read_b64_tr_b16 v[152:153], v177 offset:0xc800
	ds_read_b64_tr_b16 v[154:155], v177 offset:0xd800
	ds_read_b64_tr_b16 v[156:157], v177 offset:0xe800
	ds_read_b64_tr_b16 v[158:159], v177 offset:0xf800
	s_waitcnt lgkmcnt(8)
	v_mfma_f32_32x32x16_bf16 v[64:79], v[166:169], v[128:131], v[64:79]
	v_mfma_f32_32x32x16_bf16 v[64:79], v[178:181], v[132:135], v[64:79]
	v_mfma_f32_32x32x16_bf16 v[64:79], v[182:185], v[136:139], v[64:79]
	v_mfma_f32_32x32x16_bf16 v[64:79], v[186:189], v[140:143], v[64:79]
	ds_read_b64_tr_b16 v[166:167], v177 offset:0x8a00
	ds_read_b64_tr_b16 v[168:169], v177 offset:0x9a00
	ds_read_b64_tr_b16 v[178:179], v177 offset:0xaa00
	ds_read_b64_tr_b16 v[180:181], v177 offset:0xba00
	ds_read_b64_tr_b16 v[182:183], v177 offset:0xca00
	ds_read_b64_tr_b16 v[184:185], v177 offset:0xda00
	ds_read_b64_tr_b16 v[186:187], v177 offset:0xea00
	ds_read_b64_tr_b16 v[188:189], v177 offset:0xfa00
	s_waitcnt lgkmcnt(8)
	v_mfma_f32_32x32x16_bf16 v[48:63], v[144:147], v[128:131], v[48:63]
	v_mfma_f32_32x32x16_bf16 v[48:63], v[148:151], v[132:135], v[48:63]
	v_mfma_f32_32x32x16_bf16 v[48:63], v[152:155], v[136:139], v[48:63]
	v_mfma_f32_32x32x16_bf16 v[48:63], v[156:159], v[140:143], v[48:63]
	ds_read_b64_tr_b16 v[144:145], v177 offset:0x8c00
	ds_read_b64_tr_b16 v[146:147], v177 offset:0x9c00
	ds_read_b64_tr_b16 v[148:149], v177 offset:0xac00
	ds_read_b64_tr_b16 v[150:151], v177 offset:0xbc00
	ds_read_b64_tr_b16 v[152:153], v177 offset:0xcc00
	ds_read_b64_tr_b16 v[154:155], v177 offset:0xdc00
	ds_read_b64_tr_b16 v[156:157], v177 offset:0xec00
	ds_read_b64_tr_b16 v[158:159], v177 offset:0xfc00
	s_waitcnt lgkmcnt(8)
	v_mfma_f32_32x32x16_bf16 v[32:47], v[166:169], v[128:131], v[32:47]
	v_mfma_f32_32x32x16_bf16 v[32:47], v[178:181], v[132:135], v[32:47]
	v_mfma_f32_32x32x16_bf16 v[32:47], v[182:185], v[136:139], v[32:47]
	v_mfma_f32_32x32x16_bf16 v[32:47], v[186:189], v[140:143], v[32:47]
	ds_read_b64_tr_b16 v[166:167], v177 offset:0x8e00
	ds_read_b64_tr_b16 v[168:169], v177 offset:0x9e00
	ds_read_b64_tr_b16 v[178:179], v177 offset:0xae00
	ds_read_b64_tr_b16 v[180:181], v177 offset:0xbe00
	ds_read_b64_tr_b16 v[182:183], v177 offset:0xce00
	ds_read_b64_tr_b16 v[184:185], v177 offset:0xde00
	ds_read_b64_tr_b16 v[186:187], v177 offset:0xee00
	ds_read_b64_tr_b16 v[188:189], v177 offset:0xfe00
	s_waitcnt lgkmcnt(8)
	v_mfma_f32_32x32x16_bf16 v[16:31], v[144:147], v[128:131], v[16:31]
	v_mfma_f32_32x32x16_bf16 v[16:31], v[148:151], v[132:135], v[16:31]
	v_mfma_f32_32x32x16_bf16 v[16:31], v[152:155], v[136:139], v[16:31]
	v_mfma_f32_32x32x16_bf16 v[16:31], v[156:159], v[140:143], v[16:31]
	s_waitcnt lgkmcnt(0)
	v_mfma_f32_32x32x16_bf16 v[0:15], v[166:169], v[128:131], v[0:15]
	v_mfma_f32_32x32x16_bf16 v[0:15], v[178:181], v[132:135], v[0:15]
	v_mfma_f32_32x32x16_bf16 v[0:15], v[182:185], v[136:139], v[0:15]
	v_mfma_f32_32x32x16_bf16 v[0:15], v[186:189], v[140:143], v[0:15]
	v_readlane_b32 s2, v255, 46
	v_readlane_b32 s3, v255, 47
	s_ashr_i32 s93, s92, 31
	v_or_b32_e32 v160, v175, v160
	v_mov_b64_e32 v[128:129], s[2:3]
	v_readlane_b32 s2, v255, 54
	v_readlane_b32 s3, v255, 55
	flat_load_dword v130, v[128:129] sc0 sc1
	v_mov_b64_e32 v[128:129], s[2:3]
	flat_load_dword v128, v[128:129] sc0 sc1
	s_waitcnt vmcnt(0) lgkmcnt(0)
	v_readfirstlane_b32 s4, v130
	s_mul_i32 s3, s92, 0x6800
	s_mul_hi_i32 s2, s92, 0x6800
	s_add_u32 s4, s4, s3
	s_waitcnt lgkmcnt(0)
	s_barrier
	s_waitcnt lgkmcnt(0)
	v_readfirstlane_b32 s5, v128
	s_addc_u32 s5, s5, s2
	s_nop 0
	v_lshl_add_u64 v[156:157], s[4:5], 0, v[160:161]
	flat_load_dwordx4 v[128:131], v[156:157]
	flat_load_dwordx4 v[132:135], v[156:157] offset:32
	flat_load_dwordx4 v[136:139], v[156:157] offset:64
	flat_load_dwordx4 v[140:143], v[156:157] offset:96
	flat_load_dwordx4 v[144:147], v[156:157] offset:128
	flat_load_dwordx4 v[148:151], v[156:157] offset:160
	flat_load_dwordx4 v[152:155], v[156:157] offset:192
	flat_load_dwordx4 v[166:169], v[156:157] offset:224
	s_lshl_b64 s[4:5], s[92:93], 12
	s_add_u32 s4, s83, s4
	v_rcp_f32_e32 v159, v162
	s_addc_u32 s5, s95, s5
	v_lshl_or_b32 v162, v176, 12, v175
	global_load_dwordx4 v[194:197], v162, s[4:5]
	global_load_dwordx4 v[198:201], v162, s[4:5] offset:32
	global_load_dwordx4 v[202:205], v162, s[4:5] offset:64
	global_load_dwordx4 v[206:209], v162, s[4:5] offset:96
	global_load_dwordx4 v[210:213], v162, s[4:5] offset:128
	global_load_dwordx4 v[214:217], v162, s[4:5] offset:160
	global_load_dwordx4 v[218:221], v162, s[4:5] offset:192
	global_load_dwordx4 v[222:225], v162, s[4:5] offset:224
	v_mul_f32_e32 v112, v159, v112
	v_mul_f32_e32 v96, v159, v96
	v_mul_f32_e32 v80, v159, v80
	v_mul_f32_e32 v64, v159, v64
	v_mul_f32_e32 v48, v159, v48
	v_mul_f32_e32 v32, v159, v32
	v_mul_f32_e32 v16, v159, v16
	v_mul_f32_e32 v0, v159, v0
	v_readlane_b32 s18, v255, 19
	s_waitcnt vmcnt(0)
	v_mov_b32_e32 v163, v196
	s_nop 1
	v_permlane32_swap_b32_e32 v194, v163
	v_mov_b32_e32 v170, v197
	v_fma_mix_f32 v157, -v174, v112, v194 op_sel_hi:[0,0,1]
	v_mul_f32_e32 v112, v159, v113
	v_permlane32_swap_b32_e32 v195, v170
	v_fma_mix_f32 v156, -v174, v112, v194 op_sel:[0,0,1] op_sel_hi:[0,0,1]
	v_mul_f32_e32 v112, v159, v114
	v_fma_mix_f32 v113, -v174, v112, v195 op_sel_hi:[0,0,1]
	v_mul_f32_e32 v112, v159, v115
	v_fma_mix_f32 v112, -v174, v112, v195 op_sel:[0,0,1] op_sel_hi:[0,0,1]
	global_load_dwordx4 v[194:197], v162, s[4:5] offset:256
	v_mul_f32_e32 v114, v159, v116
	v_fma_mix_f32 v158, -v174, v114, v163 op_sel_hi:[0,0,1]
	v_mul_f32_e32 v114, v159, v117
	v_fma_mix_f32 v116, -v174, v114, v163 op_sel:[0,0,1] op_sel_hi:[0,0,1]
	v_mul_f32_e32 v114, v159, v118
	v_fma_mix_f32 v115, -v174, v114, v170 op_sel_hi:[0,0,1]
	v_mul_f32_e32 v114, v159, v119
	v_mul_f32_e32 v117, v159, v120
	v_fma_mix_f32 v114, -v174, v114, v170 op_sel:[0,0,1] op_sel_hi:[0,0,1]
	s_waitcnt vmcnt(7)
	v_mov_b32_e32 v163, v200
	s_nop 1
	v_permlane32_swap_b32_e32 v198, v163
	v_mov_b32_e32 v170, v201
	v_fma_mix_f32 v120, -v174, v117, v198 op_sel_hi:[0,0,1]
	v_mul_f32_e32 v117, v159, v121
	v_permlane32_swap_b32_e32 v199, v170
	v_fma_mix_f32 v119, -v174, v117, v198 op_sel:[0,0,1] op_sel_hi:[0,0,1]
	v_mul_f32_e32 v117, v159, v122
	v_fma_mix_f32 v118, -v174, v117, v199 op_sel_hi:[0,0,1]
	v_mul_f32_e32 v117, v159, v123
	v_fma_mix_f32 v117, -v174, v117, v199 op_sel:[0,0,1] op_sel_hi:[0,0,1]
	global_load_dwordx4 v[198:201], v162, s[4:5] offset:288
	v_mul_f32_e32 v121, v159, v124
	v_fma_mix_f32 v124, -v174, v121, v163 op_sel_hi:[0,0,1]
	v_mul_f32_e32 v121, v159, v125
	v_fma_mix_f32 v123, -v174, v121, v163 op_sel:[0,0,1] op_sel_hi:[0,0,1]
	v_mul_f32_e32 v121, v159, v126
	v_fma_mix_f32 v122, -v174, v121, v170 op_sel_hi:[0,0,1]
	v_mul_f32_e32 v121, v159, v127
	v_fma_mix_f32 v121, -v174, v121, v170 op_sel:[0,0,1] op_sel_hi:[0,0,1]
	s_waitcnt vmcnt(7)
	v_mov_b32_e32 v163, v204
	s_nop 1
	v_permlane32_swap_b32_e32 v202, v163
	v_mov_b32_e32 v170, v205
	v_fma_mix_f32 v126, -v174, v96, v202 op_sel_hi:[0,0,1]
	v_mul_f32_e32 v96, v159, v97
	v_permlane32_swap_b32_e32 v203, v170
	v_fma_mix_f32 v125, -v174, v96, v202 op_sel:[0,0,1] op_sel_hi:[0,0,1]
	v_mul_f32_e32 v96, v159, v98
	v_fma_mix_f32 v97, -v174, v96, v203 op_sel_hi:[0,0,1]
	v_mul_f32_e32 v96, v159, v99
	v_fma_mix_f32 v96, -v174, v96, v203 op_sel:[0,0,1] op_sel_hi:[0,0,1]
	global_load_dwordx4 v[202:205], v162, s[4:5] offset:320
	v_mul_f32_e32 v98, v159, v100
	v_fma_mix_f32 v127, -v174, v98, v163 op_sel_hi:[0,0,1]
	v_mul_f32_e32 v98, v159, v101
	v_fma_mix_f32 v100, -v174, v98, v163 op_sel:[0,0,1] op_sel_hi:[0,0,1]
	v_mul_f32_e32 v98, v159, v102
	v_fma_mix_f32 v99, -v174, v98, v170 op_sel_hi:[0,0,1]
	v_mul_f32_e32 v98, v159, v103
	v_mul_f32_e32 v101, v159, v104
	v_fma_mix_f32 v98, -v174, v98, v170 op_sel:[0,0,1] op_sel_hi:[0,0,1]
	s_waitcnt vmcnt(7)
	v_mov_b32_e32 v163, v208
	s_nop 1
	v_permlane32_swap_b32_e32 v206, v163
	v_mov_b32_e32 v170, v209
	v_fma_mix_f32 v104, -v174, v101, v206 op_sel_hi:[0,0,1]
	v_mul_f32_e32 v101, v159, v105
	v_permlane32_swap_b32_e32 v207, v170
	v_fma_mix_f32 v103, -v174, v101, v206 op_sel:[0,0,1] op_sel_hi:[0,0,1]
	v_mul_f32_e32 v101, v159, v106
	v_fma_mix_f32 v102, -v174, v101, v207 op_sel_hi:[0,0,1]
	v_mul_f32_e32 v101, v159, v107
	v_fma_mix_f32 v101, -v174, v101, v207 op_sel:[0,0,1] op_sel_hi:[0,0,1]
	global_load_dwordx4 v[206:209], v162, s[4:5] offset:352
	v_mul_f32_e32 v105, v159, v108
	v_fma_mix_f32 v108, -v174, v105, v163 op_sel_hi:[0,0,1]
	v_mul_f32_e32 v105, v159, v109
	v_fma_mix_f32 v107, -v174, v105, v163 op_sel:[0,0,1] op_sel_hi:[0,0,1]
	v_mul_f32_e32 v105, v159, v110
	v_fma_mix_f32 v106, -v174, v105, v170 op_sel_hi:[0,0,1]
	v_mul_f32_e32 v105, v159, v111
	v_fma_mix_f32 v105, -v174, v105, v170 op_sel:[0,0,1] op_sel_hi:[0,0,1]
	s_waitcnt vmcnt(7)
	v_mov_b32_e32 v163, v212
	s_nop 1
	v_permlane32_swap_b32_e32 v210, v163
	v_mov_b32_e32 v170, v213
	v_fma_mix_f32 v110, -v174, v80, v210 op_sel_hi:[0,0,1]
	v_mul_f32_e32 v80, v159, v81
	v_permlane32_swap_b32_e32 v211, v170
	v_fma_mix_f32 v109, -v174, v80, v210 op_sel:[0,0,1] op_sel_hi:[0,0,1]
	v_mul_f32_e32 v80, v159, v82
	v_fma_mix_f32 v81, -v174, v80, v211 op_sel_hi:[0,0,1]
	v_mul_f32_e32 v80, v159, v83
	v_fma_mix_f32 v80, -v174, v80, v211 op_sel:[0,0,1] op_sel_hi:[0,0,1]
	global_load_dwordx4 v[210:213], v162, s[4:5] offset:384
	v_mul_f32_e32 v82, v159, v84
	v_fma_mix_f32 v111, -v174, v82, v163 op_sel_hi:[0,0,1]
	v_mul_f32_e32 v82, v159, v85
	v_fma_mix_f32 v84, -v174, v82, v163 op_sel:[0,0,1] op_sel_hi:[0,0,1]
	v_mul_f32_e32 v82, v159, v86
	v_fma_mix_f32 v83, -v174, v82, v170 op_sel_hi:[0,0,1]
	v_mul_f32_e32 v82, v159, v87
	v_mul_f32_e32 v85, v159, v88
	v_fma_mix_f32 v82, -v174, v82, v170 op_sel:[0,0,1] op_sel_hi:[0,0,1]
	s_waitcnt vmcnt(7)
	v_mov_b32_e32 v163, v216
	s_nop 1
	v_permlane32_swap_b32_e32 v214, v163
	v_mov_b32_e32 v170, v217
	v_fma_mix_f32 v88, -v174, v85, v214 op_sel_hi:[0,0,1]
	v_mul_f32_e32 v85, v159, v89
	v_permlane32_swap_b32_e32 v215, v170
	v_fma_mix_f32 v87, -v174, v85, v214 op_sel:[0,0,1] op_sel_hi:[0,0,1]
	v_mul_f32_e32 v85, v159, v90
	v_fma_mix_f32 v86, -v174, v85, v215 op_sel_hi:[0,0,1]
	v_mul_f32_e32 v85, v159, v91
	v_fma_mix_f32 v85, -v174, v85, v215 op_sel:[0,0,1] op_sel_hi:[0,0,1]
	global_load_dwordx4 v[214:217], v162, s[4:5] offset:416
	v_mul_f32_e32 v89, v159, v92
	v_fma_mix_f32 v92, -v174, v89, v163 op_sel_hi:[0,0,1]
	v_mul_f32_e32 v89, v159, v93
	v_fma_mix_f32 v91, -v174, v89, v163 op_sel:[0,0,1] op_sel_hi:[0,0,1]
	v_mul_f32_e32 v89, v159, v94
	v_fma_mix_f32 v90, -v174, v89, v170 op_sel_hi:[0,0,1]
	v_mul_f32_e32 v89, v159, v95
	v_fma_mix_f32 v89, -v174, v89, v170 op_sel:[0,0,1] op_sel_hi:[0,0,1]
	s_waitcnt vmcnt(7)
	v_mov_b32_e32 v163, v220
	s_nop 1
	v_permlane32_swap_b32_e32 v218, v163
	v_mov_b32_e32 v170, v221
	v_fma_mix_f32 v94, -v174, v64, v218 op_sel_hi:[0,0,1]
	v_mul_f32_e32 v64, v159, v65
	v_permlane32_swap_b32_e32 v219, v170
	v_fma_mix_f32 v93, -v174, v64, v218 op_sel:[0,0,1] op_sel_hi:[0,0,1]
	v_mul_f32_e32 v64, v159, v66
	v_fma_mix_f32 v65, -v174, v64, v219 op_sel_hi:[0,0,1]
	v_mul_f32_e32 v64, v159, v67
	v_fma_mix_f32 v64, -v174, v64, v219 op_sel:[0,0,1] op_sel_hi:[0,0,1]
	global_load_dwordx4 v[218:221], v162, s[4:5] offset:448
	v_mul_f32_e32 v66, v159, v68
	v_fma_mix_f32 v95, -v174, v66, v163 op_sel_hi:[0,0,1]
	v_mul_f32_e32 v66, v159, v69
	v_fma_mix_f32 v68, -v174, v66, v163 op_sel:[0,0,1] op_sel_hi:[0,0,1]
	v_mul_f32_e32 v66, v159, v70
	v_fma_mix_f32 v67, -v174, v66, v170 op_sel_hi:[0,0,1]
	v_mul_f32_e32 v66, v159, v71
	v_mul_f32_e32 v69, v159, v72
	v_fma_mix_f32 v66, -v174, v66, v170 op_sel:[0,0,1] op_sel_hi:[0,0,1]
	s_waitcnt vmcnt(7)
	v_mov_b32_e32 v163, v224
	s_nop 1
	v_permlane32_swap_b32_e32 v222, v163
	v_mov_b32_e32 v170, v225
	v_fma_mix_f32 v72, -v174, v69, v222 op_sel_hi:[0,0,1]
	v_mul_f32_e32 v69, v159, v73
	v_permlane32_swap_b32_e32 v223, v170
	v_fma_mix_f32 v71, -v174, v69, v222 op_sel:[0,0,1] op_sel_hi:[0,0,1]
	v_mul_f32_e32 v69, v159, v74
	v_fma_mix_f32 v70, -v174, v69, v223 op_sel_hi:[0,0,1]
	v_mul_f32_e32 v69, v159, v75
	v_fma_mix_f32 v69, -v174, v69, v223 op_sel:[0,0,1] op_sel_hi:[0,0,1]
	v_mul_f32_e32 v73, v159, v76
	v_fma_mix_f32 v76, -v174, v73, v163 op_sel_hi:[0,0,1]
	v_mul_f32_e32 v73, v159, v77
	v_fma_mix_f32 v75, -v174, v73, v163 op_sel:[0,0,1] op_sel_hi:[0,0,1]
	v_mul_f32_e32 v73, v159, v78
	v_fma_mix_f32 v74, -v174, v73, v170 op_sel_hi:[0,0,1]
	v_mul_f32_e32 v73, v159, v79
	v_fma_mix_f32 v73, -v174, v73, v170 op_sel:[0,0,1] op_sel_hi:[0,0,1]
	s_waitcnt vmcnt(6)
	v_mov_b32_e32 v163, v196
	s_nop 1
	v_permlane32_swap_b32_e32 v194, v163
	v_mov_b32_e32 v170, v197
	v_fma_mix_f32 v78, -v174, v48, v194 op_sel_hi:[0,0,1]
	v_mul_f32_e32 v48, v159, v49
	v_permlane32_swap_b32_e32 v195, v170
	v_fma_mix_f32 v77, -v174, v48, v194 op_sel:[0,0,1] op_sel_hi:[0,0,1]
	v_mul_f32_e32 v48, v159, v50
	v_fma_mix_f32 v49, -v174, v48, v195 op_sel_hi:[0,0,1]
	v_mul_f32_e32 v48, v159, v51
	v_fma_mix_f32 v48, -v174, v48, v195 op_sel:[0,0,1] op_sel_hi:[0,0,1]
	v_mul_f32_e32 v50, v159, v52
	v_fma_mix_f32 v79, -v174, v50, v163 op_sel_hi:[0,0,1]
	v_mul_f32_e32 v50, v159, v53
	v_fma_mix_f32 v52, -v174, v50, v163 op_sel:[0,0,1] op_sel_hi:[0,0,1]
	v_mul_f32_e32 v50, v159, v54
	v_fma_mix_f32 v51, -v174, v50, v170 op_sel_hi:[0,0,1]
	v_mul_f32_e32 v50, v159, v55
	v_mul_f32_e32 v53, v159, v56
	v_fma_mix_f32 v50, -v174, v50, v170 op_sel:[0,0,1] op_sel_hi:[0,0,1]
	s_waitcnt vmcnt(5)
	v_mov_b32_e32 v163, v200
	s_nop 1
	v_permlane32_swap_b32_e32 v198, v163
	v_mov_b32_e32 v170, v201
	v_fma_mix_f32 v56, -v174, v53, v198 op_sel_hi:[0,0,1]
	v_mul_f32_e32 v53, v159, v57
	v_permlane32_swap_b32_e32 v199, v170
	v_fma_mix_f32 v55, -v174, v53, v198 op_sel:[0,0,1] op_sel_hi:[0,0,1]
	v_mul_f32_e32 v53, v159, v58
	v_fma_mix_f32 v54, -v174, v53, v199 op_sel_hi:[0,0,1]
	v_mul_f32_e32 v53, v159, v59
	v_fma_mix_f32 v53, -v174, v53, v199 op_sel:[0,0,1] op_sel_hi:[0,0,1]
	v_mul_f32_e32 v57, v159, v60
	v_fma_mix_f32 v60, -v174, v57, v163 op_sel_hi:[0,0,1]
	v_mul_f32_e32 v57, v159, v61
	v_fma_mix_f32 v59, -v174, v57, v163 op_sel:[0,0,1] op_sel_hi:[0,0,1]
	v_mul_f32_e32 v57, v159, v62
	v_fma_mix_f32 v58, -v174, v57, v170 op_sel_hi:[0,0,1]
	v_mul_f32_e32 v57, v159, v63
	v_fma_mix_f32 v57, -v174, v57, v170 op_sel:[0,0,1] op_sel_hi:[0,0,1]
	s_waitcnt vmcnt(4)
	v_mov_b32_e32 v163, v204
	s_nop 1
	v_permlane32_swap_b32_e32 v202, v163
	v_mov_b32_e32 v170, v205
	v_fma_mix_f32 v62, -v174, v32, v202 op_sel_hi:[0,0,1]
	v_mul_f32_e32 v32, v159, v33
	v_permlane32_swap_b32_e32 v203, v170
	v_fma_mix_f32 v61, -v174, v32, v202 op_sel:[0,0,1] op_sel_hi:[0,0,1]
	v_mul_f32_e32 v32, v159, v34
	v_fma_mix_f32 v33, -v174, v32, v203 op_sel_hi:[0,0,1]
	v_mul_f32_e32 v32, v159, v35
	v_fma_mix_f32 v32, -v174, v32, v203 op_sel:[0,0,1] op_sel_hi:[0,0,1]
	v_mul_f32_e32 v34, v159, v36
	v_fma_mix_f32 v63, -v174, v34, v163 op_sel_hi:[0,0,1]
	v_mul_f32_e32 v34, v159, v37
	v_fma_mix_f32 v36, -v174, v34, v163 op_sel:[0,0,1] op_sel_hi:[0,0,1]
	v_mul_f32_e32 v34, v159, v38
	v_fma_mix_f32 v35, -v174, v34, v170 op_sel_hi:[0,0,1]
	v_mul_f32_e32 v34, v159, v39
	v_mul_f32_e32 v37, v159, v40
	v_fma_mix_f32 v34, -v174, v34, v170 op_sel:[0,0,1] op_sel_hi:[0,0,1]
	s_waitcnt vmcnt(3)
	v_mov_b32_e32 v163, v208
	s_nop 1
	v_permlane32_swap_b32_e32 v206, v163
	v_mov_b32_e32 v170, v209
	v_fma_mix_f32 v40, -v174, v37, v206 op_sel_hi:[0,0,1]
	v_mul_f32_e32 v37, v159, v41
	v_permlane32_swap_b32_e32 v207, v170
	v_fma_mix_f32 v39, -v174, v37, v206 op_sel:[0,0,1] op_sel_hi:[0,0,1]
	v_mul_f32_e32 v37, v159, v42
	v_fma_mix_f32 v38, -v174, v37, v207 op_sel_hi:[0,0,1]
	v_mul_f32_e32 v37, v159, v43
	v_fma_mix_f32 v37, -v174, v37, v207 op_sel:[0,0,1] op_sel_hi:[0,0,1]
	v_mul_f32_e32 v41, v159, v44
	v_fma_mix_f32 v44, -v174, v41, v163 op_sel_hi:[0,0,1]
	v_mul_f32_e32 v41, v159, v45
	v_fma_mix_f32 v43, -v174, v41, v163 op_sel:[0,0,1] op_sel_hi:[0,0,1]
	v_mul_f32_e32 v41, v159, v46
	v_fma_mix_f32 v42, -v174, v41, v170 op_sel_hi:[0,0,1]
	v_mul_f32_e32 v41, v159, v47
	v_fma_mix_f32 v41, -v174, v41, v170 op_sel:[0,0,1] op_sel_hi:[0,0,1]
	s_waitcnt vmcnt(2)
	v_mov_b32_e32 v163, v212
	s_nop 1
	v_permlane32_swap_b32_e32 v210, v163
	v_mov_b32_e32 v170, v213
	v_fma_mix_f32 v46, -v174, v16, v210 op_sel_hi:[0,0,1]
	v_mul_f32_e32 v16, v159, v17
	v_permlane32_swap_b32_e32 v211, v170
	v_fma_mix_f32 v45, -v174, v16, v210 op_sel:[0,0,1] op_sel_hi:[0,0,1]
	v_mul_f32_e32 v16, v159, v18
	v_fma_mix_f32 v17, -v174, v16, v211 op_sel_hi:[0,0,1]
	v_mul_f32_e32 v16, v159, v19
	v_fma_mix_f32 v16, -v174, v16, v211 op_sel:[0,0,1] op_sel_hi:[0,0,1]
	v_mul_f32_e32 v18, v159, v20
	v_fma_mix_f32 v47, -v174, v18, v163 op_sel_hi:[0,0,1]
	v_mul_f32_e32 v18, v159, v21
	v_fma_mix_f32 v20, -v174, v18, v163 op_sel:[0,0,1] op_sel_hi:[0,0,1]
	v_mul_f32_e32 v18, v159, v22
	v_fma_mix_f32 v19, -v174, v18, v170 op_sel_hi:[0,0,1]
	v_mul_f32_e32 v18, v159, v23
	v_mul_f32_e32 v21, v159, v24
	v_fma_mix_f32 v18, -v174, v18, v170 op_sel:[0,0,1] op_sel_hi:[0,0,1]
	s_waitcnt vmcnt(1)
	v_mov_b32_e32 v163, v216
	s_nop 1
	v_permlane32_swap_b32_e32 v214, v163
	v_mov_b32_e32 v170, v217
	v_fma_mix_f32 v24, -v174, v21, v214 op_sel_hi:[0,0,1]
	v_mul_f32_e32 v21, v159, v25
	v_permlane32_swap_b32_e32 v215, v170
	v_fma_mix_f32 v23, -v174, v21, v214 op_sel:[0,0,1] op_sel_hi:[0,0,1]
	v_mul_f32_e32 v21, v159, v26
	v_fma_mix_f32 v22, -v174, v21, v215 op_sel_hi:[0,0,1]
	v_mul_f32_e32 v21, v159, v27
	v_fma_mix_f32 v21, -v174, v21, v215 op_sel:[0,0,1] op_sel_hi:[0,0,1]
	v_mul_f32_e32 v25, v159, v28
	v_fma_mix_f32 v28, -v174, v25, v163 op_sel_hi:[0,0,1]
	v_mul_f32_e32 v25, v159, v29
	v_fma_mix_f32 v27, -v174, v25, v163 op_sel:[0,0,1] op_sel_hi:[0,0,1]
	v_mul_f32_e32 v25, v159, v30
	v_fma_mix_f32 v26, -v174, v25, v170 op_sel_hi:[0,0,1]
	v_mul_f32_e32 v25, v159, v31
	v_fma_mix_f32 v25, -v174, v25, v170 op_sel:[0,0,1] op_sel_hi:[0,0,1]
	s_waitcnt vmcnt(0)
	v_mov_b32_e32 v170, v220
	s_nop 1
	v_permlane32_swap_b32_e32 v218, v170
	v_mov_b32_e32 v172, v221
	v_fma_mix_f32 v163, -v174, v0, v218 op_sel_hi:[0,0,1]
	v_mul_f32_e32 v0, v159, v1
	v_permlane32_swap_b32_e32 v219, v172
	v_fma_mix_f32 v31, -v174, v0, v218 op_sel:[0,0,1] op_sel_hi:[0,0,1]
	v_mul_f32_e32 v0, v159, v2
	v_fma_mix_f32 v30, -v174, v0, v219 op_sel_hi:[0,0,1]
	v_mul_f32_e32 v0, v159, v3
	v_fma_mix_f32 v29, -v174, v0, v219 op_sel:[0,0,1] op_sel_hi:[0,0,1]
	v_mul_f32_e32 v0, v159, v4
	v_fma_mix_f32 v171, -v174, v0, v170 op_sel_hi:[0,0,1]
	v_mul_f32_e32 v0, v159, v5
	v_fma_mix_f32 v170, -v174, v0, v170 op_sel:[0,0,1] op_sel_hi:[0,0,1]
	v_mul_f32_e32 v0, v159, v6
	v_fma_mix_f32 v5, -v174, v0, v172 op_sel_hi:[0,0,1]
	v_mul_f32_e32 v0, v159, v7
	v_fma_mix_f32 v4, -v174, v0, v172 op_sel:[0,0,1] op_sel_hi:[0,0,1]
	global_load_dwordx4 v[0:3], v162, s[4:5] offset:480
	s_add_u32 s4, s6, s3
	v_readlane_b32 s3, v255, 16
	s_addc_u32 s5, s3, s2
	v_readlane_b32 s2, v255, 28
	s_waitcnt vmcnt(0)
	v_mov_b32_e32 v7, v2
	s_nop 1
	v_permlane32_swap_b32_e32 v0, v7
	v_mul_f32_e32 v2, v159, v8
	v_mov_b32_e32 v162, v3
	v_fma_mix_f32 v6, -v174, v2, v0 op_sel_hi:[0,0,1]
	v_mul_f32_e32 v2, v159, v9
	v_permlane32_swap_b32_e32 v1, v162
	v_fma_mix_f32 v3, -v174, v2, v0 op_sel:[0,0,1] op_sel_hi:[0,0,1]
	v_mul_f32_e32 v0, v159, v10
	v_fma_mix_f32 v2, -v174, v0, v1 op_sel_hi:[0,0,1]
	v_mul_f32_e32 v0, v159, v11
	v_mul_f32_e32 v10, v156, v156
	v_mul_f32_e32 v11, v112, v112
	v_fmac_f32_e32 v10, v157, v157
	v_fmac_f32_e32 v11, v113, v113
	v_fma_mix_f32 v0, -v174, v0, v1 op_sel:[0,0,1] op_sel_hi:[0,0,1]
	v_mul_f32_e32 v1, v159, v12
	v_add_f32_e32 v10, v10, v11
	v_mul_f32_e32 v11, v116, v116
	v_mul_f32_e32 v12, v114, v114
	v_fmac_f32_e32 v11, v158, v158
	v_fmac_f32_e32 v12, v115, v115
	v_fma_mix_f32 v9, -v174, v1, v7 op_sel_hi:[0,0,1]
	v_mul_f32_e32 v1, v159, v13
	v_add_f32_e32 v11, v11, v12
	v_mul_f32_e32 v12, v119, v119
	v_mul_f32_e32 v13, v117, v117
	v_fmac_f32_e32 v12, v120, v120
	v_fmac_f32_e32 v13, v118, v118
	v_fma_mix_f32 v8, -v174, v1, v7 op_sel:[0,0,1] op_sel_hi:[0,0,1]
	v_mul_f32_e32 v1, v159, v14
	v_add_f32_e32 v12, v12, v13
	v_mul_f32_e32 v13, v123, v123
	v_mul_f32_e32 v14, v121, v121
	v_fmac_f32_e32 v13, v124, v124
	v_fmac_f32_e32 v14, v122, v122
	v_add_f32_e32 v13, v13, v14
	v_add_f32_e32 v10, v10, v11
	v_add_f32_e32 v11, v12, v13
	v_add_f32_e32 v10, v10, v11
	v_mul_f32_e32 v11, v125, v125
	v_mul_f32_e32 v12, v96, v96
	v_fmac_f32_e32 v11, v126, v126
	v_fmac_f32_e32 v12, v97, v97
	v_add_f32_e32 v11, v11, v12
	v_mul_f32_e32 v12, v100, v100
	v_mul_f32_e32 v13, v98, v98
	v_fmac_f32_e32 v12, v127, v127
	v_fmac_f32_e32 v13, v99, v99
	v_add_f32_e32 v12, v12, v13
	v_mul_f32_e32 v13, v103, v103
	v_mul_f32_e32 v14, v101, v101
	v_fmac_f32_e32 v13, v104, v104
	v_fmac_f32_e32 v14, v102, v102
	v_fma_mix_f32 v7, -v174, v1, v162 op_sel_hi:[0,0,1]
	v_mul_f32_e32 v1, v159, v15
	v_add_f32_e32 v13, v13, v14
	v_mul_f32_e32 v14, v107, v107
	v_mul_f32_e32 v15, v105, v105
	v_fmac_f32_e32 v14, v108, v108
	v_fmac_f32_e32 v15, v106, v106
	v_add_f32_e32 v14, v14, v15
	v_add_f32_e32 v11, v11, v12
	v_add_f32_e32 v12, v13, v14
	v_add_f32_e32 v11, v11, v12
	v_add_f32_e32 v10, v10, v11
	v_mul_f32_e32 v11, v109, v109
	v_mul_f32_e32 v12, v80, v80
	v_fmac_f32_e32 v11, v110, v110
	v_fmac_f32_e32 v12, v81, v81
	v_add_f32_e32 v11, v11, v12
	v_mul_f32_e32 v12, v84, v84
	v_mul_f32_e32 v13, v82, v82
	v_fmac_f32_e32 v12, v111, v111
	v_fmac_f32_e32 v13, v83, v83
	v_add_f32_e32 v12, v12, v13
	v_mul_f32_e32 v13, v87, v87
	v_mul_f32_e32 v14, v85, v85
	v_fmac_f32_e32 v13, v88, v88
	v_fmac_f32_e32 v14, v86, v86
	v_add_f32_e32 v13, v13, v14
	v_mul_f32_e32 v14, v91, v91
	v_mul_f32_e32 v15, v89, v89
	v_fmac_f32_e32 v14, v92, v92
	v_fmac_f32_e32 v15, v90, v90
	v_add_f32_e32 v14, v14, v15
	v_add_f32_e32 v11, v11, v12
	v_add_f32_e32 v12, v13, v14
	v_add_f32_e32 v11, v11, v12
	v_add_f32_e32 v10, v10, v11
	v_mul_f32_e32 v11, v93, v93
	v_mul_f32_e32 v12, v64, v64
	v_fmac_f32_e32 v11, v94, v94
	v_fmac_f32_e32 v12, v65, v65
	v_add_f32_e32 v11, v11, v12
	v_mul_f32_e32 v12, v68, v68
	v_mul_f32_e32 v13, v66, v66
	v_fmac_f32_e32 v12, v95, v95
	v_fmac_f32_e32 v13, v67, v67
	v_add_f32_e32 v12, v12, v13
	v_mul_f32_e32 v13, v71, v71
	v_mul_f32_e32 v14, v69, v69
	v_fmac_f32_e32 v13, v72, v72
	v_fmac_f32_e32 v14, v70, v70
	v_add_f32_e32 v13, v13, v14
	v_mul_f32_e32 v14, v75, v75
	v_mul_f32_e32 v15, v73, v73
	v_fmac_f32_e32 v14, v76, v76
	v_fmac_f32_e32 v15, v74, v74
	v_add_f32_e32 v14, v14, v15
	v_add_f32_e32 v11, v11, v12
	v_add_f32_e32 v12, v13, v14
	v_add_f32_e32 v11, v11, v12
	v_add_f32_e32 v10, v10, v11
	v_mul_f32_e32 v11, v77, v77
	v_mul_f32_e32 v12, v48, v48
	v_fmac_f32_e32 v11, v78, v78
	v_fmac_f32_e32 v12, v49, v49
	v_add_f32_e32 v11, v11, v12
	v_mul_f32_e32 v12, v52, v52
	v_mul_f32_e32 v13, v50, v50
	v_fmac_f32_e32 v12, v79, v79
	v_fmac_f32_e32 v13, v51, v51
	v_add_f32_e32 v12, v12, v13
	v_mul_f32_e32 v13, v55, v55
	v_mul_f32_e32 v14, v53, v53
	v_fmac_f32_e32 v13, v56, v56
	v_fmac_f32_e32 v14, v54, v54
	v_add_f32_e32 v13, v13, v14
	v_mul_f32_e32 v14, v59, v59
	v_mul_f32_e32 v15, v57, v57
	v_fmac_f32_e32 v14, v60, v60
	v_fmac_f32_e32 v15, v58, v58
	v_add_f32_e32 v14, v14, v15
	v_add_f32_e32 v11, v11, v12
	v_add_f32_e32 v12, v13, v14
	v_add_f32_e32 v11, v11, v12
	v_add_f32_e32 v10, v10, v11
	v_mul_f32_e32 v11, v61, v61
	v_mul_f32_e32 v12, v32, v32
	v_fmac_f32_e32 v11, v62, v62
	v_fmac_f32_e32 v12, v33, v33
	v_add_f32_e32 v11, v11, v12
	v_mul_f32_e32 v12, v36, v36
	v_mul_f32_e32 v13, v34, v34
	v_fmac_f32_e32 v12, v63, v63
	v_fmac_f32_e32 v13, v35, v35
	v_add_f32_e32 v12, v12, v13
	v_mul_f32_e32 v13, v39, v39
	v_mul_f32_e32 v14, v37, v37
	v_fmac_f32_e32 v13, v40, v40
	v_fmac_f32_e32 v14, v38, v38
	v_add_f32_e32 v13, v13, v14
	v_mul_f32_e32 v14, v43, v43
	v_mul_f32_e32 v15, v41, v41
	v_fmac_f32_e32 v14, v44, v44
	v_fmac_f32_e32 v15, v42, v42
	v_add_f32_e32 v14, v14, v15
	v_add_f32_e32 v11, v11, v12
	v_add_f32_e32 v12, v13, v14
	v_add_f32_e32 v11, v11, v12
	v_add_f32_e32 v10, v10, v11
	v_mul_f32_e32 v11, v45, v45
	v_mul_f32_e32 v12, v16, v16
	v_fmac_f32_e32 v11, v46, v46
	v_fmac_f32_e32 v12, v17, v17
	v_add_f32_e32 v11, v11, v12
	v_mul_f32_e32 v12, v20, v20
	v_mul_f32_e32 v13, v18, v18
	v_fmac_f32_e32 v12, v47, v47
	v_fmac_f32_e32 v13, v19, v19
	v_add_f32_e32 v12, v12, v13
	v_mul_f32_e32 v13, v23, v23
	v_mul_f32_e32 v14, v21, v21
	v_fmac_f32_e32 v13, v24, v24
	v_fmac_f32_e32 v14, v22, v22
	v_add_f32_e32 v13, v13, v14
	v_mul_f32_e32 v14, v27, v27
	v_mul_f32_e32 v15, v25, v25
	v_fmac_f32_e32 v14, v28, v28
	v_fmac_f32_e32 v15, v26, v26
	v_add_f32_e32 v14, v14, v15
	v_add_f32_e32 v11, v11, v12
	v_add_f32_e32 v12, v13, v14
	v_add_f32_e32 v11, v11, v12
	v_add_f32_e32 v10, v10, v11
	v_mul_f32_e32 v11, v31, v31
	v_mul_f32_e32 v12, v29, v29
	v_fmac_f32_e32 v11, v163, v163
	v_fmac_f32_e32 v12, v30, v30
	v_add_f32_e32 v11, v11, v12
	v_mul_f32_e32 v12, v170, v170
	v_mul_f32_e32 v13, v4, v4
	v_fmac_f32_e32 v12, v171, v171
	v_fmac_f32_e32 v13, v5, v5
	v_add_f32_e32 v12, v12, v13
	v_mul_f32_e32 v13, v3, v3
	v_mul_f32_e32 v14, v0, v0
	v_fma_mix_f32 v1, -v174, v1, v162 op_sel:[0,0,1] op_sel_hi:[0,0,1]
	v_fmac_f32_e32 v13, v6, v6
	v_fmac_f32_e32 v14, v2, v2
	v_add_f32_e32 v13, v13, v14
	v_mul_f32_e32 v14, v8, v8
	v_mul_f32_e32 v15, v1, v1
	v_fmac_f32_e32 v14, v9, v9
	v_fmac_f32_e32 v15, v7, v7
	v_add_f32_e32 v14, v14, v15
	v_add_f32_e32 v11, v11, v12
	v_add_f32_e32 v12, v13, v14
	v_add_f32_e32 v11, v11, v12
	v_add_f32_e32 v10, v10, v11
	v_mov_b32_e32 v11, v10
	s_nop 1
	v_permlane32_swap_b32_e32 v10, v11
	v_add_f32_e32 v10, v10, v11
	v_fmamk_f32 v10, v10, 0x3b800000, v254
	v_rsq_f32_e32 v10, v10
	v_add_u32_e32 v11, s2, v175
	ds_read_b128 v[12:15], v11
	ds_read_b128 v[176:179], v11 offset:32
	v_readlane_b32 s2, v255, 20
	v_mul_f32_e32 v10, v173, v10
	v_mul_f32_e32 v157, v157, v10
	v_mul_f32_e32 v156, v156, v10
	v_mul_f32_e32 v113, v113, v10
	v_mul_f32_e32 v112, v112, v10
	s_waitcnt lgkmcnt(0)
	v_mul_f32_e32 v12, v12, v157
	v_mul_f32_e32 v157, v158, v10
	v_mul_f32_e32 v13, v13, v156
	v_mul_f32_e32 v116, v116, v10
	v_mul_f32_e32 v14, v14, v113
	v_mul_f32_e32 v113, v115, v10
	v_mul_f32_e32 v15, v15, v112
	v_mul_f32_e32 v112, v114, v10
	v_mul_f32_e32 v157, v176, v157
	v_mul_f32_e32 v116, v177, v116
	v_mul_f32_e32 v113, v178, v113
	v_mul_f32_e32 v112, v179, v112
	v_cvt_pk_bf16_f32 v12, v12, v13
	v_cvt_pk_bf16_f32 v13, v14, v15
	v_cvt_pk_bf16_f32 v14, v157, v116
	v_cvt_pk_bf16_f32 v15, v113, v112
	v_mul_f32_e32 v116, v120, v10
	v_permlane32_swap_b32_e32 v12, v14
	v_permlane32_swap_b32_e32 v13, v15
	global_store_dwordx4 v160, v[12:15], s[4:5]
	ds_read_b128 v[12:15], v11 offset:64
	ds_read_b128 v[112:115], v11 offset:96
	v_mul_f32_e32 v97, v97, v10
	v_mul_f32_e32 v96, v96, v10
	v_mul_f32_e32 v100, v100, v10
	s_waitcnt lgkmcnt(1)
	v_mul_f32_e32 v12, v116, v12
	v_mul_f32_e32 v116, v124, v10
	s_waitcnt lgkmcnt(0)
	v_mul_f32_e32 v112, v116, v112
	v_mul_f32_e32 v116, v119, v10
	v_mul_f32_e32 v13, v116, v13
	v_mul_f32_e32 v116, v123, v10
	v_mul_f32_e32 v113, v116, v113
	v_mul_f32_e32 v116, v118, v10
	v_mul_f32_e32 v14, v116, v14
	v_mul_f32_e32 v116, v122, v10
	v_mul_f32_e32 v114, v116, v114
	v_mul_f32_e32 v116, v117, v10
	v_mul_f32_e32 v15, v116, v15
	v_mul_f32_e32 v116, v121, v10
	v_mul_f32_e32 v115, v116, v115
	v_cvt_pk_bf16_f32 v12, v12, v13
	v_cvt_pk_bf16_f32 v13, v14, v15
	v_cvt_pk_bf16_f32 v14, v112, v113
	v_cvt_pk_bf16_f32 v15, v114, v115
	v_mul_f32_e32 v116, v126, v10
	v_permlane32_swap_b32_e32 v12, v14
	v_permlane32_swap_b32_e32 v13, v15
	global_store_dwordx4 v160, v[12:15], s[4:5] offset:32
	ds_read_b128 v[12:15], v11 offset:128
	ds_read_b128 v[112:115], v11 offset:160
	v_mul_f32_e32 v81, v81, v10
	v_mul_f32_e32 v80, v80, v10
	v_mul_f32_e32 v84, v84, v10
	s_waitcnt lgkmcnt(1)
	v_mul_f32_e32 v12, v116, v12
	v_mul_f32_e32 v116, v127, v10
	s_waitcnt lgkmcnt(0)
	v_mul_f32_e32 v112, v116, v112
	v_mul_f32_e32 v116, v125, v10
	v_mul_f32_e32 v13, v116, v13
	v_mul_f32_e32 v14, v97, v14
	v_mul_f32_e32 v97, v99, v10
	v_mul_f32_e32 v15, v96, v15
	v_mul_f32_e32 v96, v98, v10
	v_mul_f32_e32 v100, v100, v113
	v_mul_f32_e32 v97, v97, v114
	v_mul_f32_e32 v96, v96, v115
	v_cvt_pk_bf16_f32 v12, v12, v13
	v_cvt_pk_bf16_f32 v13, v14, v15
	v_cvt_pk_bf16_f32 v14, v112, v100
	v_cvt_pk_bf16_f32 v15, v97, v96
	v_mul_f32_e32 v100, v104, v10
	v_permlane32_swap_b32_e32 v12, v14
	v_permlane32_swap_b32_e32 v13, v15
	global_store_dwordx4 v160, v[12:15], s[4:5] offset:64
	ds_read_b128 v[12:15], v11 offset:192
	ds_read_b128 v[96:99], v11 offset:224
	v_mul_f32_e32 v65, v65, v10
	v_mul_f32_e32 v64, v64, v10
	v_mul_f32_e32 v68, v68, v10
	s_waitcnt lgkmcnt(1)
	v_mul_f32_e32 v12, v100, v12
	v_mul_f32_e32 v100, v108, v10
	s_waitcnt lgkmcnt(0)
	v_mul_f32_e32 v96, v100, v96
	v_mul_f32_e32 v100, v103, v10
	v_mul_f32_e32 v13, v100, v13
	v_mul_f32_e32 v100, v107, v10
	v_mul_f32_e32 v97, v100, v97
	v_mul_f32_e32 v100, v102, v10
	v_mul_f32_e32 v14, v100, v14
	v_mul_f32_e32 v100, v106, v10
	v_mul_f32_e32 v98, v100, v98
	v_mul_f32_e32 v100, v101, v10
	v_mul_f32_e32 v15, v100, v15
	v_mul_f32_e32 v100, v105, v10
	v_mul_f32_e32 v99, v100, v99
	v_cvt_pk_bf16_f32 v12, v12, v13
	v_cvt_pk_bf16_f32 v13, v14, v15
	v_cvt_pk_bf16_f32 v14, v96, v97
	v_cvt_pk_bf16_f32 v15, v98, v99
	v_or_b32_e32 v96, 64, v160
	v_permlane32_swap_b32_e32 v12, v14
	v_permlane32_swap_b32_e32 v13, v15
	global_store_dwordx4 v96, v[12:15], s[4:5] offset:32
	ds_read_b128 v[12:15], v11 offset:256
	ds_read_b128 v[96:99], v11 offset:288
	v_mul_f32_e32 v100, v110, v10
	v_mul_f32_e32 v49, v49, v10
	v_mul_f32_e32 v48, v48, v10
	s_waitcnt lgkmcnt(1)
	v_mul_f32_e32 v12, v100, v12
	v_mul_f32_e32 v100, v111, v10
	s_waitcnt lgkmcnt(0)
	v_mul_f32_e32 v96, v100, v96
	v_mul_f32_e32 v100, v109, v10
	v_mul_f32_e32 v13, v100, v13
	v_mul_f32_e32 v14, v81, v14
	v_mul_f32_e32 v81, v83, v10
	v_mul_f32_e32 v15, v80, v15
	v_mul_f32_e32 v80, v82, v10
	v_mul_f32_e32 v84, v84, v97
	v_mul_f32_e32 v81, v81, v98
	v_mul_f32_e32 v80, v80, v99
	v_cvt_pk_bf16_f32 v12, v12, v13
	v_cvt_pk_bf16_f32 v13, v14, v15
	v_cvt_pk_bf16_f32 v14, v96, v84
	v_cvt_pk_bf16_f32 v15, v81, v80
	v_mul_f32_e32 v84, v88, v10
	v_permlane32_swap_b32_e32 v12, v14
	v_permlane32_swap_b32_e32 v13, v15
	global_store_dwordx4 v160, v[12:15], s[4:5] offset:128
	ds_read_b128 v[12:15], v11 offset:320
	ds_read_b128 v[80:83], v11 offset:352
	v_mul_f32_e32 v52, v52, v10
	v_mul_f32_e32 v33, v33, v10
	v_mul_f32_e32 v32, v32, v10
	s_waitcnt lgkmcnt(1)
	v_mul_f32_e32 v12, v84, v12
	v_mul_f32_e32 v84, v92, v10
	s_waitcnt lgkmcnt(0)
	v_mul_f32_e32 v80, v84, v80
	v_mul_f32_e32 v84, v87, v10
	v_mul_f32_e32 v13, v84, v13
	v_mul_f32_e32 v84, v91, v10
	v_mul_f32_e32 v81, v84, v81
	v_mul_f32_e32 v84, v86, v10
	v_mul_f32_e32 v14, v84, v14
	v_mul_f32_e32 v84, v90, v10
	v_mul_f32_e32 v82, v84, v82
	v_mul_f32_e32 v84, v85, v10
	v_mul_f32_e32 v15, v84, v15
	v_mul_f32_e32 v84, v89, v10
	v_mul_f32_e32 v83, v84, v83
	v_cvt_pk_bf16_f32 v12, v12, v13
	v_cvt_pk_bf16_f32 v13, v14, v15
	v_cvt_pk_bf16_f32 v14, v80, v81
	v_cvt_pk_bf16_f32 v15, v82, v83
	v_or_b32_e32 v80, 0x80, v160
	v_permlane32_swap_b32_e32 v12, v14
	v_permlane32_swap_b32_e32 v13, v15
	global_store_dwordx4 v80, v[12:15], s[4:5] offset:32
	ds_read_b128 v[12:15], v11 offset:384
	ds_read_b128 v[80:83], v11 offset:416
	v_mul_f32_e32 v84, v94, v10
	v_mul_f32_e32 v36, v36, v10
	v_mul_f32_e32 v17, v17, v10
	s_waitcnt lgkmcnt(1)
	v_mul_f32_e32 v12, v84, v12
	v_mul_f32_e32 v84, v95, v10
	s_waitcnt lgkmcnt(0)
	v_mul_f32_e32 v80, v84, v80
	v_mul_f32_e32 v84, v93, v10
	v_mul_f32_e32 v13, v84, v13
	v_mul_f32_e32 v14, v65, v14
	v_mul_f32_e32 v65, v67, v10
	v_mul_f32_e32 v15, v64, v15
	v_mul_f32_e32 v64, v66, v10
	v_mul_f32_e32 v68, v68, v81
	v_mul_f32_e32 v65, v65, v82
	v_mul_f32_e32 v64, v64, v83
	v_cvt_pk_bf16_f32 v12, v12, v13
	v_cvt_pk_bf16_f32 v13, v14, v15
	v_cvt_pk_bf16_f32 v14, v80, v68
	v_cvt_pk_bf16_f32 v15, v65, v64
	v_mul_f32_e32 v68, v72, v10
	v_permlane32_swap_b32_e32 v12, v14
	v_permlane32_swap_b32_e32 v13, v15
	global_store_dwordx4 v160, v[12:15], s[4:5] offset:192
	ds_read_b128 v[12:15], v11 offset:448
	ds_read_b128 v[64:67], v11 offset:480
	v_mul_f32_e32 v16, v16, v10
	v_mul_f32_e32 v20, v20, v10
	v_mul_f32_e32 v5, v5, v10
	s_waitcnt lgkmcnt(1)
	v_mul_f32_e32 v12, v68, v12
	v_mul_f32_e32 v68, v76, v10
	s_waitcnt lgkmcnt(0)
	v_mul_f32_e32 v64, v68, v64
	v_mul_f32_e32 v68, v71, v10
	v_mul_f32_e32 v13, v68, v13
	v_mul_f32_e32 v68, v75, v10
	v_mul_f32_e32 v65, v68, v65
	v_mul_f32_e32 v68, v70, v10
	v_mul_f32_e32 v14, v68, v14
	v_mul_f32_e32 v68, v74, v10
	v_mul_f32_e32 v66, v68, v66
	v_mul_f32_e32 v68, v69, v10
	v_mul_f32_e32 v15, v68, v15
	v_mul_f32_e32 v68, v73, v10
	v_mul_f32_e32 v67, v68, v67
	v_cvt_pk_bf16_f32 v12, v12, v13
	v_cvt_pk_bf16_f32 v13, v14, v15
	v_cvt_pk_bf16_f32 v14, v64, v65
	v_cvt_pk_bf16_f32 v15, v66, v67
	v_or_b32_e32 v64, 0xc0, v160
	v_permlane32_swap_b32_e32 v12, v14
	v_permlane32_swap_b32_e32 v13, v15
	global_store_dwordx4 v64, v[12:15], s[4:5] offset:32
	ds_read_b128 v[12:15], v11 offset:512
	ds_read_b128 v[64:67], v11 offset:544
	v_mul_f32_e32 v68, v78, v10
	v_mul_f32_e32 v4, v4, v10
	v_mul_f32_e32 v3, v3, v10
	s_waitcnt lgkmcnt(1)
	v_mul_f32_e32 v12, v68, v12
	v_mul_f32_e32 v68, v79, v10
	s_waitcnt lgkmcnt(0)
	v_mul_f32_e32 v64, v68, v64
	v_mul_f32_e32 v68, v77, v10
	v_mul_f32_e32 v13, v68, v13
	v_mul_f32_e32 v14, v49, v14
	v_mul_f32_e32 v49, v51, v10
	v_mul_f32_e32 v15, v48, v15
	v_mul_f32_e32 v48, v50, v10
	v_mul_f32_e32 v52, v52, v65
	v_mul_f32_e32 v49, v49, v66
	v_mul_f32_e32 v48, v48, v67
	v_cvt_pk_bf16_f32 v12, v12, v13
	v_cvt_pk_bf16_f32 v13, v14, v15
	v_cvt_pk_bf16_f32 v14, v64, v52
	v_cvt_pk_bf16_f32 v15, v49, v48
	v_mul_f32_e32 v52, v56, v10
	v_permlane32_swap_b32_e32 v12, v14
	v_permlane32_swap_b32_e32 v13, v15
	global_store_dwordx4 v160, v[12:15], s[4:5] offset:256
	ds_read_b128 v[12:15], v11 offset:576
	ds_read_b128 v[48:51], v11 offset:608
	v_mul_f32_e32 v2, v2, v10
	v_mul_f32_e32 v0, v0, v10
	v_mul_f32_e32 v7, v7, v10
	s_waitcnt lgkmcnt(1)
	v_mul_f32_e32 v12, v52, v12
	v_mul_f32_e32 v52, v60, v10
	s_waitcnt lgkmcnt(0)
	v_mul_f32_e32 v48, v52, v48
	v_mul_f32_e32 v52, v55, v10
	v_mul_f32_e32 v13, v52, v13
	v_mul_f32_e32 v52, v59, v10
	v_mul_f32_e32 v49, v52, v49
	v_mul_f32_e32 v52, v54, v10
	v_mul_f32_e32 v14, v52, v14
	v_mul_f32_e32 v52, v58, v10
	v_mul_f32_e32 v50, v52, v50
	v_mul_f32_e32 v52, v53, v10
	v_mul_f32_e32 v15, v52, v15
	v_mul_f32_e32 v52, v57, v10
	v_mul_f32_e32 v51, v52, v51
	v_cvt_pk_bf16_f32 v12, v12, v13
	v_cvt_pk_bf16_f32 v13, v14, v15
	v_cvt_pk_bf16_f32 v14, v48, v49
	v_cvt_pk_bf16_f32 v15, v50, v51
	v_or_b32_e32 v48, 0x100, v160
	v_permlane32_swap_b32_e32 v12, v14
	v_permlane32_swap_b32_e32 v13, v15
	global_store_dwordx4 v48, v[12:15], s[4:5] offset:32
	ds_read_b128 v[12:15], v11 offset:640
	ds_read_b128 v[48:51], v11 offset:672
	v_mul_f32_e32 v52, v62, v10
	s_cmp_lt_u32 s94, s2
	s_waitcnt lgkmcnt(1)
	v_mul_f32_e32 v12, v52, v12
	v_mul_f32_e32 v52, v63, v10
	s_waitcnt lgkmcnt(0)
	v_mul_f32_e32 v48, v52, v48
	v_mul_f32_e32 v52, v61, v10
	v_mul_f32_e32 v13, v52, v13
	v_mul_f32_e32 v14, v33, v14
	v_mul_f32_e32 v33, v35, v10
	v_mul_f32_e32 v15, v32, v15
	v_mul_f32_e32 v32, v34, v10
	v_mul_f32_e32 v36, v36, v49
	v_mul_f32_e32 v33, v33, v50
	v_mul_f32_e32 v32, v32, v51
	v_cvt_pk_bf16_f32 v12, v12, v13
	v_cvt_pk_bf16_f32 v13, v14, v15
	v_cvt_pk_bf16_f32 v14, v48, v36
	v_cvt_pk_bf16_f32 v15, v33, v32
	v_mul_f32_e32 v36, v40, v10
	v_permlane32_swap_b32_e32 v12, v14
	v_permlane32_swap_b32_e32 v13, v15
	global_store_dwordx4 v160, v[12:15], s[4:5] offset:320
	ds_read_b128 v[12:15], v11 offset:704
	ds_read_b128 v[32:35], v11 offset:736
	s_waitcnt lgkmcnt(1)
	v_mul_f32_e32 v12, v36, v12
	v_mul_f32_e32 v36, v44, v10
	s_waitcnt lgkmcnt(0)
	v_mul_f32_e32 v32, v36, v32
	v_mul_f32_e32 v36, v39, v10
	v_mul_f32_e32 v13, v36, v13
	v_mul_f32_e32 v36, v43, v10
	v_mul_f32_e32 v33, v36, v33
	v_mul_f32_e32 v36, v38, v10
	v_mul_f32_e32 v14, v36, v14
	v_mul_f32_e32 v36, v42, v10
	v_mul_f32_e32 v34, v36, v34
	v_mul_f32_e32 v36, v37, v10
	v_mul_f32_e32 v15, v36, v15
	v_mul_f32_e32 v36, v41, v10
	v_mul_f32_e32 v35, v36, v35
	v_cvt_pk_bf16_f32 v12, v12, v13
	v_cvt_pk_bf16_f32 v13, v14, v15
	v_cvt_pk_bf16_f32 v14, v32, v33
	v_cvt_pk_bf16_f32 v15, v34, v35
	v_or_b32_e32 v32, 0x140, v160
	v_permlane32_swap_b32_e32 v12, v14
	v_permlane32_swap_b32_e32 v13, v15
	global_store_dwordx4 v32, v[12:15], s[4:5] offset:32
	ds_read_b128 v[12:15], v11 offset:768
	ds_read_b128 v[32:35], v11 offset:800
	v_mul_f32_e32 v36, v46, v10
	s_waitcnt lgkmcnt(1)
	v_mul_f32_e32 v12, v36, v12
	v_mul_f32_e32 v36, v47, v10
	s_waitcnt lgkmcnt(0)
	v_mul_f32_e32 v32, v36, v32
	v_mul_f32_e32 v36, v45, v10
	v_mul_f32_e32 v13, v36, v13
	v_mul_f32_e32 v14, v17, v14
	v_mul_f32_e32 v17, v19, v10
	v_mul_f32_e32 v15, v16, v15
	v_mul_f32_e32 v16, v18, v10
	v_mul_f32_e32 v20, v20, v33
	v_mul_f32_e32 v17, v17, v34
	v_mul_f32_e32 v16, v16, v35
	v_cvt_pk_bf16_f32 v12, v12, v13
	v_cvt_pk_bf16_f32 v13, v14, v15
	v_cvt_pk_bf16_f32 v14, v32, v20
	v_cvt_pk_bf16_f32 v15, v17, v16
	v_mul_f32_e32 v20, v24, v10
	v_permlane32_swap_b32_e32 v12, v14
	v_permlane32_swap_b32_e32 v13, v15
	global_store_dwordx4 v160, v[12:15], s[4:5] offset:384
	ds_read_b128 v[12:15], v11 offset:832
	ds_read_b128 v[16:19], v11 offset:864
	s_waitcnt lgkmcnt(1)
	v_mul_f32_e32 v12, v20, v12
	v_mul_f32_e32 v20, v28, v10
	s_waitcnt lgkmcnt(0)
	v_mul_f32_e32 v16, v20, v16
	v_mul_f32_e32 v20, v23, v10
	v_mul_f32_e32 v13, v20, v13
	v_mul_f32_e32 v20, v27, v10
	v_mul_f32_e32 v17, v20, v17
	v_mul_f32_e32 v20, v22, v10
	v_mul_f32_e32 v14, v20, v14
	v_mul_f32_e32 v20, v26, v10
	v_mul_f32_e32 v18, v20, v18
	v_mul_f32_e32 v20, v21, v10
	v_mul_f32_e32 v15, v20, v15
	v_mul_f32_e32 v20, v25, v10
	v_mul_f32_e32 v19, v20, v19
	v_cvt_pk_bf16_f32 v12, v12, v13
	v_cvt_pk_bf16_f32 v13, v14, v15
	v_cvt_pk_bf16_f32 v14, v16, v17
	v_cvt_pk_bf16_f32 v15, v18, v19
	v_or_b32_e32 v16, 0x180, v160
	v_permlane32_swap_b32_e32 v12, v14
	v_permlane32_swap_b32_e32 v13, v15
	global_store_dwordx4 v16, v[12:15], s[4:5] offset:32
	ds_read_b128 v[12:15], v11 offset:896
	ds_read_b128 v[16:19], v11 offset:928
	v_mul_f32_e32 v20, v163, v10
	s_waitcnt lgkmcnt(1)
	v_mul_f32_e32 v12, v20, v12
	v_mul_f32_e32 v20, v171, v10
	s_waitcnt lgkmcnt(0)
	v_mul_f32_e32 v16, v20, v16
	v_mul_f32_e32 v20, v31, v10
	v_mul_f32_e32 v13, v20, v13
	v_mul_f32_e32 v20, v170, v10
	v_mul_f32_e32 v17, v20, v17
	v_mul_f32_e32 v20, v30, v10
	v_mul_f32_e32 v5, v5, v18
	v_mul_f32_e32 v18, v29, v10
	v_mul_f32_e32 v14, v20, v14
	v_mul_f32_e32 v15, v18, v15
	v_mul_f32_e32 v4, v4, v19
	v_cvt_pk_bf16_f32 v12, v12, v13
	v_cvt_pk_bf16_f32 v13, v14, v15
	v_cvt_pk_bf16_f32 v14, v16, v17
	v_cvt_pk_bf16_f32 v15, v5, v4
	v_mul_f32_e32 v4, v6, v10
	v_permlane32_swap_b32_e32 v12, v14
	v_permlane32_swap_b32_e32 v13, v15
	global_store_dwordx4 v160, v[12:15], s[4:5] offset:448
	ds_read_b128 v[12:15], v11 offset:960
	ds_read_b128 v[16:19], v11 offset:992
	v_mul_f32_e32 v5, v9, v10
	v_mul_f32_e32 v6, v8, v10
	s_waitcnt lgkmcnt(1)
	v_mul_f32_e32 v3, v3, v13
	v_mul_f32_e32 v2, v2, v14
	v_mul_f32_e32 v8, v0, v15
	v_mul_f32_e32 v0, v1, v10
	v_mul_f32_e32 v4, v4, v12
	s_waitcnt lgkmcnt(0)
	v_mul_f32_e32 v5, v5, v16
	v_mul_f32_e32 v6, v6, v17
	v_mul_f32_e32 v7, v7, v18
	v_mul_f32_e32 v9, v0, v19
	v_cvt_pk_bf16_f32 v0, v4, v3
	v_cvt_pk_bf16_f32 v1, v2, v8
	v_cvt_pk_bf16_f32 v2, v5, v6
	v_cvt_pk_bf16_f32 v3, v7, v9
	v_or_b32_e32 v4, 0x1c0, v160
	v_permlane32_swap_b32_e32 v0, v2
	v_permlane32_swap_b32_e32 v1, v3
	global_store_dwordx4 v4, v[0:3], s[4:5] offset:32
	s_cbranch_scc0 .LBB0_616

.LBB0_584:
	s_lshl_b64 s[2:3], s[94:95], 12
	v_readlane_b32 s4, v255, 43
	s_add_u32 s2, s4, s2
	v_readlane_b32 s4, v255, 44
	s_addc_u32 s3, s4, s3
	v_readlane_b32 s4, v255, 17
	s_add_u32 s83, s2, s4
	s_addc_u32 s95, s3, 0
	v_add_f32_e32 v162, v144, v145
	v_fmac_f32_e32 v162, v178, v160
	v_mul_u32_u24_e32 v160, 0x6800, v175
	ds_read_b64_tr_b16 v[144:145], v177 offset:0x8000
	ds_read_b64_tr_b16 v[146:147], v177 offset:0x9000
	ds_read_b64_tr_b16 v[148:149], v177 offset:0xa000
	ds_read_b64_tr_b16 v[150:151], v177 offset:0xb000
	ds_read_b64_tr_b16 v[152:153], v177 offset:0xc000
	ds_read_b64_tr_b16 v[154:155], v177 offset:0xd000
	ds_read_b64_tr_b16 v[156:157], v177 offset:0xe000
	ds_read_b64_tr_b16 v[158:159], v177 offset:0xf000
	ds_read_b64_tr_b16 v[166:167], v177 offset:0x8200
	ds_read_b64_tr_b16 v[168:169], v177 offset:0x9200
	ds_read_b64_tr_b16 v[178:179], v177 offset:0xa200
	ds_read_b64_tr_b16 v[180:181], v177 offset:0xb200
	ds_read_b64_tr_b16 v[182:183], v177 offset:0xc200
	ds_read_b64_tr_b16 v[184:185], v177 offset:0xd200
	ds_read_b64_tr_b16 v[186:187], v177 offset:0xe200
	ds_read_b64_tr_b16 v[188:189], v177 offset:0xf200
	s_waitcnt lgkmcnt(8)
	s_nop 0
	v_mfma_f32_32x32x16_bf16 v[112:127], v[144:147], v[128:131], v[112:127]
	v_mfma_f32_32x32x16_bf16 v[112:127], v[148:151], v[132:135], v[112:127]
	v_mfma_f32_32x32x16_bf16 v[112:127], v[152:155], v[136:139], v[112:127]
	v_mfma_f32_32x32x16_bf16 v[112:127], v[156:159], v[140:143], v[112:127]
	ds_read_b64_tr_b16 v[144:145], v177 offset:0x8400
	ds_read_b64_tr_b16 v[146:147], v177 offset:0x9400
	ds_read_b64_tr_b16 v[148:149], v177 offset:0xa400
	ds_read_b64_tr_b16 v[150:151], v177 offset:0xb400
	ds_read_b64_tr_b16 v[152:153], v177 offset:0xc400
	ds_read_b64_tr_b16 v[154:155], v177 offset:0xd400
	ds_read_b64_tr_b16 v[156:157], v177 offset:0xe400
	ds_read_b64_tr_b16 v[158:159], v177 offset:0xf400
	s_waitcnt lgkmcnt(8)
	v_mfma_f32_32x32x16_bf16 v[80:95], v[166:169], v[128:131], v[80:95]
	v_mfma_f32_32x32x16_bf16 v[80:95], v[178:181], v[132:135], v[80:95]
	v_mfma_f32_32x32x16_bf16 v[80:95], v[182:185], v[136:139], v[80:95]
	v_mfma_f32_32x32x16_bf16 v[80:95], v[186:189], v[140:143], v[80:95]
	ds_read_b64_tr_b16 v[166:167], v177 offset:0x8600
	ds_read_b64_tr_b16 v[168:169], v177 offset:0x9600
	ds_read_b64_tr_b16 v[178:179], v177 offset:0xa600
	ds_read_b64_tr_b16 v[180:181], v177 offset:0xb600
	ds_read_b64_tr_b16 v[182:183], v177 offset:0xc600
	ds_read_b64_tr_b16 v[184:185], v177 offset:0xd600
	ds_read_b64_tr_b16 v[186:187], v177 offset:0xe600
	ds_read_b64_tr_b16 v[188:189], v177 offset:0xf600
	s_waitcnt lgkmcnt(8)
	v_mfma_f32_32x32x16_bf16 v[96:111], v[144:147], v[128:131], v[96:111]
	v_mfma_f32_32x32x16_bf16 v[96:111], v[148:151], v[132:135], v[96:111]
	v_mfma_f32_32x32x16_bf16 v[96:111], v[152:155], v[136:139], v[96:111]
	v_mfma_f32_32x32x16_bf16 v[96:111], v[156:159], v[140:143], v[96:111]
	ds_read_b64_tr_b16 v[144:145], v177 offset:0x8800
	ds_read_b64_tr_b16 v[146:147], v177 offset:0x9800
	ds_read_b64_tr_b16 v[148:149], v177 offset:0xa800
	ds_read_b64_tr_b16 v[150:151], v177 offset:0xb800
	ds_read_b64_tr_b16 v[152:153], v177 offset:0xc800
	ds_read_b64_tr_b16 v[154:155], v177 offset:0xd800
	ds_read_b64_tr_b16 v[156:157], v177 offset:0xe800
	ds_read_b64_tr_b16 v[158:159], v177 offset:0xf800
	s_waitcnt lgkmcnt(8)
	v_mfma_f32_32x32x16_bf16 v[64:79], v[166:169], v[128:131], v[64:79]
	v_mfma_f32_32x32x16_bf16 v[64:79], v[178:181], v[132:135], v[64:79]
	v_mfma_f32_32x32x16_bf16 v[64:79], v[182:185], v[136:139], v[64:79]
	v_mfma_f32_32x32x16_bf16 v[64:79], v[186:189], v[140:143], v[64:79]
	ds_read_b64_tr_b16 v[166:167], v177 offset:0x8a00
	ds_read_b64_tr_b16 v[168:169], v177 offset:0x9a00
	ds_read_b64_tr_b16 v[178:179], v177 offset:0xaa00
	ds_read_b64_tr_b16 v[180:181], v177 offset:0xba00
	ds_read_b64_tr_b16 v[182:183], v177 offset:0xca00
	ds_read_b64_tr_b16 v[184:185], v177 offset:0xda00
	ds_read_b64_tr_b16 v[186:187], v177 offset:0xea00
	ds_read_b64_tr_b16 v[188:189], v177 offset:0xfa00
	s_waitcnt lgkmcnt(8)
	v_mfma_f32_32x32x16_bf16 v[48:63], v[144:147], v[128:131], v[48:63]
	v_mfma_f32_32x32x16_bf16 v[48:63], v[148:151], v[132:135], v[48:63]
	v_mfma_f32_32x32x16_bf16 v[48:63], v[152:155], v[136:139], v[48:63]
	v_mfma_f32_32x32x16_bf16 v[48:63], v[156:159], v[140:143], v[48:63]
	ds_read_b64_tr_b16 v[144:145], v177 offset:0x8c00
	ds_read_b64_tr_b16 v[146:147], v177 offset:0x9c00
	ds_read_b64_tr_b16 v[148:149], v177 offset:0xac00
	ds_read_b64_tr_b16 v[150:151], v177 offset:0xbc00
	ds_read_b64_tr_b16 v[152:153], v177 offset:0xcc00
	ds_read_b64_tr_b16 v[154:155], v177 offset:0xdc00
	ds_read_b64_tr_b16 v[156:157], v177 offset:0xec00
	ds_read_b64_tr_b16 v[158:159], v177 offset:0xfc00
	s_waitcnt lgkmcnt(8)
	v_mfma_f32_32x32x16_bf16 v[32:47], v[166:169], v[128:131], v[32:47]
	v_mfma_f32_32x32x16_bf16 v[32:47], v[178:181], v[132:135], v[32:47]
	v_mfma_f32_32x32x16_bf16 v[32:47], v[182:185], v[136:139], v[32:47]
	v_mfma_f32_32x32x16_bf16 v[32:47], v[186:189], v[140:143], v[32:47]
	ds_read_b64_tr_b16 v[166:167], v177 offset:0x8e00
	ds_read_b64_tr_b16 v[168:169], v177 offset:0x9e00
	ds_read_b64_tr_b16 v[178:179], v177 offset:0xae00
	ds_read_b64_tr_b16 v[180:181], v177 offset:0xbe00
	ds_read_b64_tr_b16 v[182:183], v177 offset:0xce00
	ds_read_b64_tr_b16 v[184:185], v177 offset:0xde00
	ds_read_b64_tr_b16 v[186:187], v177 offset:0xee00
	ds_read_b64_tr_b16 v[188:189], v177 offset:0xfe00
	s_waitcnt lgkmcnt(8)
	v_mfma_f32_32x32x16_bf16 v[16:31], v[144:147], v[128:131], v[16:31]
	v_mfma_f32_32x32x16_bf16 v[16:31], v[148:151], v[132:135], v[16:31]
	v_mfma_f32_32x32x16_bf16 v[16:31], v[152:155], v[136:139], v[16:31]
	v_mfma_f32_32x32x16_bf16 v[16:31], v[156:159], v[140:143], v[16:31]
	s_waitcnt lgkmcnt(0)
	v_mfma_f32_32x32x16_bf16 v[0:15], v[166:169], v[128:131], v[0:15]
	v_mfma_f32_32x32x16_bf16 v[0:15], v[178:181], v[132:135], v[0:15]
	v_mfma_f32_32x32x16_bf16 v[0:15], v[182:185], v[136:139], v[0:15]
	v_mfma_f32_32x32x16_bf16 v[0:15], v[186:189], v[140:143], v[0:15]
	v_readlane_b32 s2, v255, 46
	v_readlane_b32 s3, v255, 47
	s_ashr_i32 s93, s92, 31
	v_or_b32_e32 v160, v176, v160
	v_mov_b64_e32 v[128:129], s[2:3]
	v_readlane_b32 s2, v255, 54
	v_readlane_b32 s3, v255, 55
	flat_load_dword v130, v[128:129] sc0 sc1
	v_mov_b64_e32 v[128:129], s[2:3]
	flat_load_dword v128, v[128:129] sc0 sc1
	s_waitcnt vmcnt(0) lgkmcnt(0)
	v_readfirstlane_b32 s5, v130
	s_mul_i32 s2, s92, 0x6800
	s_mul_hi_i32 s3, s92, 0x6800
	s_add_u32 s2, s5, s2
	s_waitcnt lgkmcnt(0)
	s_barrier
	s_waitcnt lgkmcnt(0)
	v_readfirstlane_b32 s4, v128
	s_addc_u32 s3, s4, s3
	v_lshl_add_u64 v[156:157], s[2:3], 0, v[160:161]
	flat_load_dwordx4 v[128:131], v[156:157]
	flat_load_dwordx4 v[132:135], v[156:157] offset:32
	flat_load_dwordx4 v[136:139], v[156:157] offset:64
	flat_load_dwordx4 v[140:143], v[156:157] offset:96
	flat_load_dwordx4 v[144:147], v[156:157] offset:128
	flat_load_dwordx4 v[148:151], v[156:157] offset:160
	flat_load_dwordx4 v[152:155], v[156:157] offset:192
	flat_load_dwordx4 v[166:169], v[156:157] offset:224
	v_rcp_f32_e32 v156, v162
	s_lshl_b64 s[2:3], s[92:93], 12
	s_add_u32 s4, s83, s2
	s_addc_u32 s5, s95, s3
	v_mul_f32_e32 v80, v156, v80
	v_mul_f32_e32 v81, v156, v81
	v_cvt_pk_f16_f32 v80, v80, v81
	v_mul_f32_e32 v81, v156, v82
	v_mul_f32_e32 v82, v156, v83
	v_cvt_pk_f16_f32 v81, v81, v82
	v_mul_f32_e32 v82, v156, v84
	v_mul_f32_e32 v83, v156, v85
	v_cvt_pk_f16_f32 v82, v82, v83
	v_mul_f32_e32 v83, v156, v86
	v_mul_f32_e32 v84, v156, v87
	v_cvt_pk_f16_f32 v83, v83, v84
	v_lshl_or_b32 v157, v175, 12, v176
	v_permlane32_swap_b32_e32 v80, v82
	v_permlane32_swap_b32_e32 v81, v83
	global_store_dwordx4 v157, v[80:83], s[4:5] offset:64
	v_mul_f32_e32 v84, v156, v95
	v_mul_f32_e32 v112, v156, v112
	v_mul_f32_e32 v80, v156, v88
	v_mul_f32_e32 v81, v156, v89
	v_cvt_pk_f16_f32 v80, v80, v81
	v_mul_f32_e32 v81, v156, v90
	v_mul_f32_e32 v82, v156, v91
	v_cvt_pk_f16_f32 v81, v81, v82
	v_mul_f32_e32 v82, v156, v92
	v_mul_f32_e32 v83, v156, v93
	v_cvt_pk_f16_f32 v82, v82, v83
	v_mul_f32_e32 v83, v156, v94
	v_cvt_pk_f16_f32 v83, v83, v84
	v_permlane32_swap_b32_e32 v80, v82
	s_nop 0
	v_permlane32_swap_b32_e32 v81, v83
	v_mul_f32_e32 v113, v156, v113
	global_store_dwordx4 v157, v[80:83], s[4:5] offset:96
	v_mul_f32_e32 v64, v156, v64
	v_mul_f32_e32 v65, v156, v65
	v_mul_f32_e32 v80, v156, v96
	v_mul_f32_e32 v81, v156, v97
	v_mul_f32_e32 v48, v156, v48
	v_mul_f32_e32 v49, v156, v49
	v_mul_f32_e32 v32, v156, v32
	v_mul_f32_e32 v33, v156, v33
	v_mul_f32_e32 v16, v156, v16
	v_mul_f32_e32 v17, v156, v17
	v_mul_f32_e32 v0, v156, v0
	v_mul_f32_e32 v1, v156, v1
	v_cvt_pk_f16_f32 v112, v112, v113
	v_mul_f32_e32 v113, v156, v114
	v_mul_f32_e32 v114, v156, v115
	v_cvt_pk_f16_f32 v80, v80, v81
	v_mul_f32_e32 v81, v156, v98
	v_mul_f32_e32 v82, v156, v99
	v_cvt_pk_f16_f32 v64, v64, v65
	v_mul_f32_e32 v65, v156, v66
	v_mul_f32_e32 v66, v156, v67
	v_cvt_pk_f16_f32 v48, v48, v49
	v_mul_f32_e32 v49, v156, v50
	v_mul_f32_e32 v50, v156, v51
	v_cvt_pk_f16_f32 v32, v32, v33
	v_mul_f32_e32 v33, v156, v34
	v_mul_f32_e32 v34, v156, v35
	v_cvt_pk_f16_f32 v16, v16, v17
	v_mul_f32_e32 v17, v156, v18
	v_mul_f32_e32 v18, v156, v19
	v_cvt_pk_f16_f32 v0, v0, v1
	v_mul_f32_e32 v1, v156, v2
	v_mul_f32_e32 v2, v156, v3
	v_cvt_pk_f16_f32 v113, v113, v114
	v_mul_f32_e32 v114, v156, v116
	v_mul_f32_e32 v115, v156, v117
	v_cvt_pk_f16_f32 v81, v81, v82
	v_mul_f32_e32 v82, v156, v100
	v_mul_f32_e32 v83, v156, v101
	v_cvt_pk_f16_f32 v65, v65, v66
	v_mul_f32_e32 v66, v156, v68
	v_mul_f32_e32 v67, v156, v69
	v_cvt_pk_f16_f32 v49, v49, v50
	v_mul_f32_e32 v50, v156, v52
	v_mul_f32_e32 v51, v156, v53
	v_cvt_pk_f16_f32 v33, v33, v34
	v_mul_f32_e32 v34, v156, v36
	v_mul_f32_e32 v35, v156, v37
	v_cvt_pk_f16_f32 v17, v17, v18
	v_mul_f32_e32 v18, v156, v20
	v_mul_f32_e32 v19, v156, v21
	v_cvt_pk_f16_f32 v1, v1, v2
	v_mul_f32_e32 v2, v156, v4
	v_mul_f32_e32 v3, v156, v5
	v_cvt_pk_f16_f32 v114, v114, v115
	v_mul_f32_e32 v115, v156, v118
	v_mul_f32_e32 v116, v156, v119
	v_cvt_pk_f16_f32 v82, v82, v83
	v_mul_f32_e32 v83, v156, v102
	v_mul_f32_e32 v84, v156, v103
	v_cvt_pk_f16_f32 v66, v66, v67
	v_mul_f32_e32 v67, v156, v70
	v_mul_f32_e32 v68, v156, v71
	v_cvt_pk_f16_f32 v50, v50, v51
	v_mul_f32_e32 v51, v156, v54
	v_mul_f32_e32 v52, v156, v55
	v_cvt_pk_f16_f32 v34, v34, v35
	v_mul_f32_e32 v35, v156, v38
	v_mul_f32_e32 v36, v156, v39
	v_cvt_pk_f16_f32 v18, v18, v19
	v_mul_f32_e32 v19, v156, v22
	v_mul_f32_e32 v20, v156, v23
	v_cvt_pk_f16_f32 v2, v2, v3
	v_mul_f32_e32 v3, v156, v6
	v_mul_f32_e32 v4, v156, v7
	v_cvt_pk_f16_f32 v115, v115, v116
	v_cvt_pk_f16_f32 v83, v83, v84
	v_cvt_pk_f16_f32 v67, v67, v68
	v_cvt_pk_f16_f32 v51, v51, v52
	v_cvt_pk_f16_f32 v35, v35, v36
	v_cvt_pk_f16_f32 v19, v19, v20
	v_cvt_pk_f16_f32 v3, v3, v4
	v_permlane32_swap_b32_e32 v112, v114
	v_permlane32_swap_b32_e32 v113, v115
	v_permlane32_swap_b32_e32 v80, v82
	v_permlane32_swap_b32_e32 v81, v83
	v_permlane32_swap_b32_e32 v64, v66
	v_permlane32_swap_b32_e32 v65, v67
	v_permlane32_swap_b32_e32 v48, v50
	v_permlane32_swap_b32_e32 v49, v51
	v_permlane32_swap_b32_e32 v32, v34
	v_permlane32_swap_b32_e32 v33, v35
	v_permlane32_swap_b32_e32 v16, v18
	v_permlane32_swap_b32_e32 v17, v19
	v_permlane32_swap_b32_e32 v0, v2
	v_permlane32_swap_b32_e32 v1, v3
	global_store_dwordx4 v157, v[112:115], s[4:5]
	global_store_dwordx4 v157, v[80:83], s[4:5] offset:128
	global_store_dwordx4 v157, v[64:67], s[4:5] offset:192
	v_mul_f32_e32 v112, v156, v120
	v_mul_f32_e32 v113, v156, v121
	v_mul_f32_e32 v80, v156, v104
	v_mul_f32_e32 v81, v156, v105
	v_mul_f32_e32 v64, v156, v72
	v_mul_f32_e32 v65, v156, v73
	global_store_dwordx4 v157, v[48:51], s[4:5] offset:256
	global_store_dwordx4 v157, v[32:35], s[4:5] offset:320
	global_store_dwordx4 v157, v[16:19], s[4:5] offset:384
	v_mul_f32_e32 v48, v156, v56
	v_mul_f32_e32 v49, v156, v57
	v_mul_f32_e32 v32, v156, v40
	v_mul_f32_e32 v33, v156, v41
	v_mul_f32_e32 v16, v156, v24
	v_mul_f32_e32 v17, v156, v25
	global_store_dwordx4 v157, v[0:3], s[4:5] offset:448
	v_cvt_pk_f16_f32 v112, v112, v113
	v_mul_f32_e32 v113, v156, v122
	v_mul_f32_e32 v0, v156, v8
	v_mul_f32_e32 v1, v156, v9
	v_mul_f32_e32 v114, v156, v123
	v_cvt_pk_f16_f32 v80, v80, v81
	v_mul_f32_e32 v81, v156, v106
	v_mul_f32_e32 v82, v156, v107
	v_cvt_pk_f16_f32 v64, v64, v65
	v_mul_f32_e32 v65, v156, v74
	v_mul_f32_e32 v66, v156, v75
	v_cvt_pk_f16_f32 v48, v48, v49
	v_mul_f32_e32 v49, v156, v58
	v_mul_f32_e32 v50, v156, v59
	v_cvt_pk_f16_f32 v32, v32, v33
	v_mul_f32_e32 v33, v156, v42
	v_mul_f32_e32 v34, v156, v43
	v_cvt_pk_f16_f32 v16, v16, v17
	v_mul_f32_e32 v17, v156, v26
	v_mul_f32_e32 v18, v156, v27
	v_cvt_pk_f16_f32 v0, v0, v1
	v_mul_f32_e32 v1, v156, v10
	v_mul_f32_e32 v2, v156, v11
	v_cvt_pk_f16_f32 v113, v113, v114
	v_mul_f32_e32 v114, v156, v124
	v_mul_f32_e32 v115, v156, v125
	v_cvt_pk_f16_f32 v81, v81, v82
	v_mul_f32_e32 v82, v156, v108
	v_mul_f32_e32 v83, v156, v109
	v_cvt_pk_f16_f32 v65, v65, v66
	v_mul_f32_e32 v66, v156, v76
	v_mul_f32_e32 v67, v156, v77
	v_cvt_pk_f16_f32 v49, v49, v50
	v_mul_f32_e32 v50, v156, v60
	v_mul_f32_e32 v51, v156, v61
	v_cvt_pk_f16_f32 v33, v33, v34
	v_mul_f32_e32 v34, v156, v44
	v_mul_f32_e32 v35, v156, v45
	v_cvt_pk_f16_f32 v17, v17, v18
	v_mul_f32_e32 v18, v156, v28
	v_mul_f32_e32 v19, v156, v29
	v_cvt_pk_f16_f32 v1, v1, v2
	v_mul_f32_e32 v2, v156, v12
	v_mul_f32_e32 v3, v156, v13
	v_cvt_pk_f16_f32 v114, v114, v115
	v_mul_f32_e32 v115, v156, v126
	v_mul_f32_e32 v116, v156, v127
	v_cvt_pk_f16_f32 v82, v82, v83
	v_mul_f32_e32 v83, v156, v110
	v_mul_f32_e32 v84, v156, v111
	v_cvt_pk_f16_f32 v66, v66, v67
	v_mul_f32_e32 v67, v156, v78
	v_mul_f32_e32 v68, v156, v79
	v_cvt_pk_f16_f32 v50, v50, v51
	v_mul_f32_e32 v51, v156, v62
	v_mul_f32_e32 v52, v156, v63
	v_cvt_pk_f16_f32 v34, v34, v35
	v_mul_f32_e32 v35, v156, v46
	v_mul_f32_e32 v36, v156, v47
	v_cvt_pk_f16_f32 v18, v18, v19
	v_mul_f32_e32 v19, v156, v30
	v_mul_f32_e32 v20, v156, v31
	v_cvt_pk_f16_f32 v2, v2, v3
	v_mul_f32_e32 v3, v156, v14
	v_mul_f32_e32 v4, v156, v15
	v_cvt_pk_f16_f32 v115, v115, v116
	v_cvt_pk_f16_f32 v83, v83, v84
	v_cvt_pk_f16_f32 v67, v67, v68
	v_cvt_pk_f16_f32 v51, v51, v52
	v_cvt_pk_f16_f32 v35, v35, v36
	v_cvt_pk_f16_f32 v19, v19, v20
	v_cvt_pk_f16_f32 v3, v3, v4
	v_permlane32_swap_b32_e32 v112, v114
	v_permlane32_swap_b32_e32 v113, v115
	v_permlane32_swap_b32_e32 v80, v82
	v_permlane32_swap_b32_e32 v81, v83
	v_permlane32_swap_b32_e32 v64, v66
	v_permlane32_swap_b32_e32 v65, v67
	v_permlane32_swap_b32_e32 v48, v50
	v_permlane32_swap_b32_e32 v49, v51
	v_permlane32_swap_b32_e32 v32, v34
	v_permlane32_swap_b32_e32 v33, v35
	v_permlane32_swap_b32_e32 v16, v18
	v_permlane32_swap_b32_e32 v17, v19
	v_permlane32_swap_b32_e32 v0, v2
	v_permlane32_swap_b32_e32 v1, v3
	s_add_i32 s94, s6, 2
	global_store_dwordx4 v157, v[112:115], s[4:5] offset:32
	global_store_dwordx4 v157, v[80:83], s[4:5] offset:160
	global_store_dwordx4 v157, v[64:67], s[4:5] offset:224
	global_store_dwordx4 v157, v[48:51], s[4:5] offset:288
	global_store_dwordx4 v157, v[32:35], s[4:5] offset:352
	global_store_dwordx4 v157, v[16:19], s[4:5] offset:416
	global_store_dwordx4 v157, v[0:3], s[4:5] offset:480
	s_mov_b64 s[4:5], exec
	v_readlane_b32 s2, v255, 49
	v_readlane_b32 s3, v255, 50
	s_and_b64 s[2:3], s[4:5], s[2:3]
	s_mov_b64 exec, s[2:3]
	s_cbranch_execz .LBB0_586
	s_or_b32 s2, s6, 1
	v_readlane_b32 s3, v255, 20
	s_cmp_lt_u32 s94, s3
	s_cselect_b32 s8, s94, s2
	s_lshr_b32 s2, s8, 2
	v_readlane_b32 s3, v255, 19
	s_mul_i32 s2, s2, s3
	v_readlane_b32 s3, v255, 18
	s_add_i32 s9, s2, s3
	s_lshl_b32 s2, s9, 6
	s_and_b32 s10, s2, 0xfffff000
	s_mul_i32 s6, s10, 0x6800
	v_readlane_b32 s15, v255, 21
	s_mul_hi_i32 s3, s10, 0x6800
	s_add_u32 s6, s15, s6
	v_readlane_b32 s16, v255, 22
	s_addc_u32 s3, s16, s3
	s_and_b32 s11, s2, 0xe00
	s_add_u32 s6, s6, s11
	s_addc_u32 s7, s3, 0
	s_add_u32 s2, s6, 0x3800
	s_addc_u32 s3, s7, 0
	s_lshl_b32 s12, s8, 8
	s_and_b32 s12, s12, 0x100
	s_add_u32 s6, s6, s12
	s_addc_u32 s7, s7, 0
	s_add_u32 s6, s6, 0x2800
	s_addc_u32 s7, s7, 0
	s_lshl_b32 s9, s9, 8
	s_and_b32 s9, s9, 0x700
	s_and_b32 s8, s8, 2
	s_xor_b32 s13, s9, 0xf00
	s_cmp_eq_u32 s8, 0
	s_cselect_b32 s8, s13, s9
	s_or_b32 s8, s8, s10
	s_mul_hi_i32 s9, s8, 0x6800
	s_mulk_i32 s8, 0x6800
	s_add_u32 s8, s15, s8
	s_addc_u32 s9, s16, s9
	s_add_u32 s8, s8, s11
	s_addc_u32 s9, s9, 0
	s_add_u32 s8, s8, s12
	s_addc_u32 s9, s9, 0
	s_add_u32 s8, s8, 0x1800
	v_readlane_b32 s10, v255, 46
	s_addc_u32 s9, s9, 0
	v_readlane_b32 s11, v255, 47
	v_mov_b64_e32 v[2:3], s[8:9]
	s_nop 0
	v_mov_b64_e32 v[0:1], s[10:11]
	ds_write_b64 v0, v[2:3]
	s_waitcnt lgkmcnt(0)
	v_mov_b64_e32 v[0:1], s[80:81]
	v_mov_b64_e32 v[2:3], s[6:7]
	ds_write_b64 v0, v[2:3]
	s_waitcnt lgkmcnt(0)
	v_mov_b64_e32 v[0:1], s[0:1]
	v_mov_b64_e32 v[2:3], s[2:3]
	ds_write_b64 v0, v[2:3]
	s_waitcnt lgkmcnt(0)
